# three GEMM phases: hipcc's 48 per-cluster s_setprio flips deleted, one static s_setprio 1 for waves 4-7 per tile loop (reset at phase exit)
# baseline (speedup 1.0000x reference)
.LBB0_161:
	v_lshl_add_u64 v[10:11], s[42:43], 0, v[210:211]
	v_mov_b32_e32 v131, v211
	v_readlane_b32 s40, v255, 17
	s_lshl_b32 s1, s1, 5
	v_lshl_add_u64 v[12:13], s[42:43], 0, v[130:131]
	v_mov_b32_e32 v135, v211
	v_readlane_b32 s41, v255, 18
	s_and_b32 s1, s1, 0x60
	s_add_i32 m0, s26, 0x18000
	v_lshl_add_u64 v[10:11], v[10:11], 0, s[36:37]
	v_lshl_add_u64 v[14:15], s[40:41], 0, v[134:135]
	v_mov_b32_e32 v133, v211
	s_lshl_b32 s10, s0, 13
	s_lshl_b32 s11, s1, 7
	s_waitcnt vmcnt(4)
	s_barrier
	global_load_lds_dwordx4 v[10:11], off
	v_lshl_add_u64 v[10:11], v[12:13], 0, s[36:37]
	s_add_i32 m0, s26, 0x1a000
	s_add_i32 s33, s26, 0x8000
	s_add_i32 s46, s26, 0xa000
	v_lshl_add_u64 v[16:17], s[40:41], 0, v[132:133]
	global_load_lds_dwordx4 v[10:11], off
	v_lshl_add_u64 v[10:11], v[14:15], 0, s[36:37]
	s_mov_b32 m0, s33
	s_add_u32 s4, s42, 0x80080
	global_load_lds_dwordx4 v[10:11], off
	v_lshl_add_u64 v[10:11], v[16:17], 0, s[36:37]
	s_mov_b32 m0, s46
	s_addc_u32 s5, s43, 0
	global_load_lds_dwordx4 v[10:11], off
	s_add_i32 m0, s26, 0x1c000
	v_lshl_add_u64 v[10:11], s[4:5], 0, v[210:211]
	global_load_lds_dwordx4 v[10:11], off
	v_lshl_add_u64 v[10:11], s[4:5], 0, v[130:131]
	s_add_i32 m0, s26, 0x1e000
	v_and_b32_e32 v9, 15, v2
	global_load_lds_dwordx4 v[10:11], off
	v_lshrrev_b32_e32 v10, 1, v2
	v_and_b32_e32 v10, 24, v10
	v_lshlrev_b32_e32 v11, 1, v10
	v_lshlrev_b32_e32 v2, 2, v2
	v_lshl_or_b32 v142, s0, 6, v9
	v_lshl_or_b32 v9, v9, 6, v11
	v_and_b32_e32 v2, 32, v2
	v_bitop3_b32 v11, v9, s10, v2 bitop3:0xde
	v_bitop3_b32 v143, v9, s11, v2 bitop3:0xde
	v_lshlrev_b32_e32 v2, 15, v7
	v_and_b32_e32 v2, 0xffff0000, v2
	v_lshl_add_u32 v2, v6, 12, v2
	v_and_b32_e32 v6, 1, v7
	v_lshl_or_b32 v2, v6, 6, v2
	v_lshl_add_u32 v136, v8, 1, v2
	v_lshlrev_b32_e32 v2, 15, v3
	v_and_b32_e32 v2, 0xffff0000, v2
	s_waitcnt vmcnt(6)
	v_lshl_add_u32 v2, v4, 12, v2
	v_and_b32_e32 v3, 1, v3
	v_or_b32_e32 v144, s1, v10
	v_lshl_or_b32 v2, v3, 6, v2
	v_readlane_b32 s0, v255, 14
	v_mov_b32_e32 v137, v211
	v_lshl_add_u32 v138, v5, 1, v2
	v_mov_b32_e32 v139, v211
	s_mov_b32 s47, 0
	v_add_u32_e32 v145, 0, v11
	v_readlane_b32 s4, v255, 16
	s_mov_b32 s5, s0
	s_barrier
	v_readlane_b32 s1, v255, 15
.LBB0_162:
	v_readfirstlane_b32 s98, v0
	s_nop 3
	s_cmp_ge_u32 s98, 0x100
	s_cbranch_scc0 .Lgp_g2
	s_setprio 1
.Lgp_g2:
	s_add_i32 s47, s47, 1
	s_mul_i32 s1, s47, s87
	s_mul_hi_u32 s11, s47, s86
	s_add_i32 s11, s11, s1
	s_mul_i32 s1, s47, s86
	s_add_u32 s24, s1, s70
	s_addc_u32 s25, s11, s71
	v_cmp_gt_i64_e64 s[38:39], s[24:25], v[214:215]
	s_and_b64 vcc, exec, s[38:39]
	s_cbranch_vccnz .LBB0_168
	s_ashr_i32 s0, s24, 31
	s_lshr_b32 s0, s0, 29
	s_add_i32 s10, s24, s0
	s_and_b32 s0, s10, -8
	s_sub_i32 s11, s24, s0
	s_cmp_gt_i32 s11, 3
	s_mov_b64 s[0:1], -1
	s_cbranch_scc0 .LBB0_165
	s_mul_i32 s0, s11, 0x165
	s_add_i32 s34, s0, 4
	s_mov_b64 s[0:1], 0

.LBB0_169:
	s_add_u32 s42, s40, 0xfff80080
	s_addc_u32 s43, s41, -1
	s_add_i32 s62, 0, 0x10000
	v_add_u32_e32 v140, s62, v143
	ds_read_b128 v[146:149], v140
	ds_read_b128 v[150:153], v140 offset:1024
	ds_read_b128 v[154:157], v140 offset:2048
	ds_read_b128 v[158:161], v140 offset:3072
	s_cmp_eq_u32 s61, 28
	s_cselect_b32 s51, s11, s43
	s_cselect_b32 s50, s52, s42
	s_cselect_b32 s43, s1, s60
	s_cselect_b32 s42, s53, s58
	v_lshl_add_u64 v[140:141], s[40:41], 0, v[136:137]
	s_add_i32 m0, s26, 0xc000
	ds_read_b128 v[162:165], v145
	ds_read_b128 v[166:169], v145 offset:1024
	ds_read_b128 v[170:173], v145 offset:2048
	ds_read_b128 v[174:177], v145 offset:3072
	ds_read_b128 v[178:181], v145 offset:4096
	ds_read_b128 v[182:185], v145 offset:5120
	ds_read_b128 v[186:189], v145 offset:6144
	ds_read_b128 v[190:193], v145 offset:7168
	global_load_lds_dwordx4 v[140:141], off
	v_lshl_add_u64 v[140:141], s[40:41], 0, v[138:139]
	s_add_i32 m0, s26, 0xe000
	s_nop 0
	global_load_lds_dwordx4 v[140:141], off
	s_waitcnt lgkmcnt(8)
	s_barrier
	s_waitcnt lgkmcnt(0)
	s_waitcnt lgkmcnt(0)
	v_mfma_f32_16x16x32_bf16 v[126:129], v[146:149], v[162:165], v[126:129]
	v_mfma_f32_16x16x32_bf16 v[122:125], v[154:157], v[162:165], v[122:125]
	v_mfma_f32_16x16x32_bf16 v[114:117], v[146:149], v[170:173], v[114:117]
	v_mfma_f32_16x16x32_bf16 v[106:109], v[154:157], v[170:173], v[106:109]
	v_mfma_f32_16x16x32_bf16 v[98:101], v[146:149], v[178:181], v[98:101]
	v_mfma_f32_16x16x32_bf16 v[90:93], v[154:157], v[178:181], v[90:93]
	v_mfma_f32_16x16x32_bf16 v[82:85], v[146:149], v[186:189], v[82:85]
	v_mfma_f32_16x16x32_bf16 v[74:77], v[154:157], v[186:189], v[74:77]
	v_mfma_f32_16x16x32_bf16 v[126:129], v[150:153], v[166:169], v[126:129]
	v_mfma_f32_16x16x32_bf16 v[122:125], v[158:161], v[166:169], v[122:125]
	v_mfma_f32_16x16x32_bf16 v[114:117], v[150:153], v[174:177], v[114:117]
	v_mfma_f32_16x16x32_bf16 v[106:109], v[158:161], v[174:177], v[106:109]
	v_mfma_f32_16x16x32_bf16 v[98:101], v[150:153], v[182:185], v[98:101]
	v_mfma_f32_16x16x32_bf16 v[90:93], v[158:161], v[182:185], v[90:93]
	v_mfma_f32_16x16x32_bf16 v[82:85], v[150:153], v[190:193], v[82:85]
	v_mfma_f32_16x16x32_bf16 v[74:77], v[158:161], v[190:193], v[74:77]
	s_barrier
	s_add_i32 s64, 0, 0x14000
	v_add_u32_e32 v140, s64, v143
	s_add_i32 s62, s62, s7
	ds_read_b128 v[194:197], v140
	ds_read_b128 v[198:201], v140 offset:1024
	ds_read_b128 v[202:205], v140 offset:2048
	ds_read_b128 v[234:237], v140 offset:3072
	v_lshl_add_u64 v[140:141], s[42:43], 0, v[210:211]
	s_mov_b32 m0, s62
	v_lshl_add_u64 v[218:219], s[42:43], 0, v[130:131]
	global_load_lds_dwordx4 v[140:141], off
	s_add_i32 m0, s62, 0x2000
	s_nop 0
	global_load_lds_dwordx4 v[218:219], off
	s_barrier
	s_waitcnt lgkmcnt(0)
	s_waitcnt lgkmcnt(0)
	v_mfma_f32_16x16x32_bf16 v[118:121], v[194:197], v[162:165], v[118:121]
	v_mfma_f32_16x16x32_bf16 v[110:113], v[202:205], v[162:165], v[110:113]
	v_mfma_f32_16x16x32_bf16 v[102:105], v[194:197], v[170:173], v[102:105]
	v_mfma_f32_16x16x32_bf16 v[94:97], v[202:205], v[170:173], v[94:97]
	v_mfma_f32_16x16x32_bf16 v[86:89], v[194:197], v[178:181], v[86:89]
	v_mfma_f32_16x16x32_bf16 v[78:81], v[202:205], v[178:181], v[78:81]
	v_mfma_f32_16x16x32_bf16 v[70:73], v[194:197], v[186:189], v[70:73]
	v_mfma_f32_16x16x32_bf16 v[66:69], v[202:205], v[186:189], v[66:69]
	v_mfma_f32_16x16x32_bf16 v[118:121], v[198:201], v[166:169], v[118:121]
	v_mfma_f32_16x16x32_bf16 v[110:113], v[234:237], v[166:169], v[110:113]
	v_mfma_f32_16x16x32_bf16 v[102:105], v[198:201], v[174:177], v[102:105]
	v_mfma_f32_16x16x32_bf16 v[94:97], v[234:237], v[174:177], v[94:97]
	v_mfma_f32_16x16x32_bf16 v[86:89], v[198:201], v[182:185], v[86:89]
	v_mfma_f32_16x16x32_bf16 v[78:81], v[234:237], v[182:185], v[78:81]
	v_mfma_f32_16x16x32_bf16 v[70:73], v[198:201], v[190:193], v[70:73]
	v_mfma_f32_16x16x32_bf16 v[66:69], v[234:237], v[190:193], v[66:69]
	s_mov_b32 m0, s26
	v_lshl_add_u64 v[238:239], s[50:51], 0, v[134:135]
	s_barrier
	ds_read_b128 v[162:165], v145 offset:16384
	ds_read_b128 v[166:169], v145 offset:17408
	ds_read_b128 v[170:173], v145 offset:18432
	ds_read_b128 v[174:177], v145 offset:19456
	ds_read_b128 v[178:181], v145 offset:20480
	ds_read_b128 v[182:185], v145 offset:21504
	ds_read_b128 v[186:189], v145 offset:22528
	ds_read_b128 v[190:193], v145 offset:23552
	global_load_lds_dwordx4 v[238:239], off
	v_lshl_add_u64 v[240:241], s[50:51], 0, v[132:133]
	s_mov_b32 m0, s27
	s_nop 0
	global_load_lds_dwordx4 v[240:241], off
	s_barrier
	s_waitcnt lgkmcnt(0)
	s_waitcnt lgkmcnt(0)
	v_mfma_f32_16x16x32_bf16 v[62:65], v[146:149], v[162:165], v[62:65]
	v_mfma_f32_16x16x32_bf16 v[58:61], v[154:157], v[162:165], v[58:61]
	v_mfma_f32_16x16x32_bf16 v[50:53], v[146:149], v[170:173], v[50:53]
	v_mfma_f32_16x16x32_bf16 v[42:45], v[154:157], v[170:173], v[42:45]
	v_mfma_f32_16x16x32_bf16 v[34:37], v[146:149], v[178:181], v[34:37]
	v_mfma_f32_16x16x32_bf16 v[26:29], v[154:157], v[178:181], v[26:29]
	v_mfma_f32_16x16x32_bf16 v[18:21], v[146:149], v[186:189], v[18:21]
	v_mfma_f32_16x16x32_bf16 v[10:13], v[154:157], v[186:189], v[10:13]
	v_mfma_f32_16x16x32_bf16 v[62:65], v[150:153], v[166:169], v[62:65]
	v_mfma_f32_16x16x32_bf16 v[58:61], v[158:161], v[166:169], v[58:61]
	v_mfma_f32_16x16x32_bf16 v[50:53], v[150:153], v[174:177], v[50:53]
	v_mfma_f32_16x16x32_bf16 v[42:45], v[158:161], v[174:177], v[42:45]
	v_mfma_f32_16x16x32_bf16 v[34:37], v[150:153], v[182:185], v[34:37]
	v_mfma_f32_16x16x32_bf16 v[26:29], v[158:161], v[182:185], v[26:29]
	v_mfma_f32_16x16x32_bf16 v[18:21], v[150:153], v[190:193], v[18:21]
	v_mfma_f32_16x16x32_bf16 v[10:13], v[158:161], v[190:193], v[10:13]
	s_barrier
	s_add_u32 s62, s42, 0x80000
	s_addc_u32 s63, s43, 0
	s_add_i32 s64, s64, s7
	v_lshl_add_u64 v[146:147], s[62:63], 0, v[210:211]
	s_mov_b32 m0, s64
	s_nop 0
	global_load_lds_dwordx4 v[146:147], off
	v_lshl_add_u64 v[146:147], s[62:63], 0, v[130:131]
	s_add_i32 m0, s64, 0x2000
	s_nop 0
	global_load_lds_dwordx4 v[146:147], off
	s_waitcnt vmcnt(6)
	s_barrier
	v_mfma_f32_16x16x32_bf16 v[54:57], v[194:197], v[162:165], v[54:57]
	v_mfma_f32_16x16x32_bf16 v[46:49], v[202:205], v[162:165], v[46:49]
	v_mfma_f32_16x16x32_bf16 v[38:41], v[194:197], v[170:173], v[38:41]
	v_mfma_f32_16x16x32_bf16 v[30:33], v[202:205], v[170:173], v[30:33]
	v_mfma_f32_16x16x32_bf16 v[22:25], v[194:197], v[178:181], v[22:25]
	v_mfma_f32_16x16x32_bf16 v[14:17], v[202:205], v[178:181], v[14:17]
	v_mfma_f32_16x16x32_bf16 v[6:9], v[194:197], v[186:189], v[6:9]
	v_mfma_f32_16x16x32_bf16 v[2:5], v[202:205], v[186:189], v[2:5]
	v_mfma_f32_16x16x32_bf16 v[54:57], v[198:201], v[166:169], v[54:57]
	v_mfma_f32_16x16x32_bf16 v[46:49], v[234:237], v[166:169], v[46:49]
	v_mfma_f32_16x16x32_bf16 v[38:41], v[198:201], v[174:177], v[38:41]
	v_mfma_f32_16x16x32_bf16 v[30:33], v[234:237], v[174:177], v[30:33]
	v_mfma_f32_16x16x32_bf16 v[22:25], v[198:201], v[182:185], v[22:25]
	v_mfma_f32_16x16x32_bf16 v[14:17], v[234:237], v[182:185], v[14:17]
	v_mfma_f32_16x16x32_bf16 v[6:9], v[198:201], v[190:193], v[6:9]
	v_mfma_f32_16x16x32_bf16 v[2:5], v[234:237], v[190:193], v[2:5]
	s_add_i32 s62, 0, 0x18000
	v_add_u32_e32 v158, s62, v143
	s_barrier
	ds_read_b128 v[146:149], v158
	ds_read_b128 v[150:153], v158 offset:1024
	ds_read_b128 v[154:157], v158 offset:2048
	ds_read_b128 v[158:161], v158 offset:3072
	s_add_u32 s50, s50, 0x80000
	s_addc_u32 s51, s51, 0
	s_mov_b32 m0, s28
	v_lshl_add_u64 v[194:195], s[50:51], 0, v[134:135]
	ds_read_b128 v[162:165], v145 offset:32768
	ds_read_b128 v[166:169], v145 offset:33792
	ds_read_b128 v[170:173], v145 offset:34816
	ds_read_b128 v[174:177], v145 offset:35840
	ds_read_b128 v[178:181], v145 offset:36864
	ds_read_b128 v[182:185], v145 offset:37888
	ds_read_b128 v[186:189], v145 offset:38912
	ds_read_b128 v[190:193], v145 offset:39936
	global_load_lds_dwordx4 v[194:195], off
	v_lshl_add_u64 v[194:195], s[50:51], 0, v[132:133]
	s_mov_b32 m0, s29
	s_nop 0
	global_load_lds_dwordx4 v[194:195], off
	s_waitcnt lgkmcnt(8)
	s_barrier
	s_waitcnt lgkmcnt(0)
	s_waitcnt lgkmcnt(0)
	v_mfma_f32_16x16x32_bf16 v[126:129], v[146:149], v[162:165], v[126:129]
	v_mfma_f32_16x16x32_bf16 v[122:125], v[154:157], v[162:165], v[122:125]
	v_mfma_f32_16x16x32_bf16 v[114:117], v[146:149], v[170:173], v[114:117]
	v_mfma_f32_16x16x32_bf16 v[106:109], v[154:157], v[170:173], v[106:109]
	v_mfma_f32_16x16x32_bf16 v[98:101], v[146:149], v[178:181], v[98:101]
	v_mfma_f32_16x16x32_bf16 v[90:93], v[154:157], v[178:181], v[90:93]
	v_mfma_f32_16x16x32_bf16 v[82:85], v[146:149], v[186:189], v[82:85]
	v_mfma_f32_16x16x32_bf16 v[74:77], v[154:157], v[186:189], v[74:77]
	v_mfma_f32_16x16x32_bf16 v[126:129], v[150:153], v[166:169], v[126:129]
	v_mfma_f32_16x16x32_bf16 v[122:125], v[158:161], v[166:169], v[122:125]
	v_mfma_f32_16x16x32_bf16 v[114:117], v[150:153], v[174:177], v[114:117]
	v_mfma_f32_16x16x32_bf16 v[106:109], v[158:161], v[174:177], v[106:109]
	v_mfma_f32_16x16x32_bf16 v[98:101], v[150:153], v[182:185], v[98:101]
	v_mfma_f32_16x16x32_bf16 v[90:93], v[158:161], v[182:185], v[90:93]
	v_mfma_f32_16x16x32_bf16 v[82:85], v[150:153], v[190:193], v[82:85]
	v_mfma_f32_16x16x32_bf16 v[74:77], v[158:161], v[190:193], v[74:77]
	s_barrier
	s_add_i32 s50, 0, 0x1c000
	s_add_i32 s51, s62, s7
	v_add_u32_e32 v226, s50, v143
	v_lshl_add_u64 v[140:141], v[140:141], 0, s[36:37]
	s_mov_b32 m0, s51
	ds_read_b128 v[194:197], v226
	ds_read_b128 v[198:201], v226 offset:1024
	ds_read_b128 v[202:205], v226 offset:2048
	ds_read_b128 v[234:237], v226 offset:3072
	global_load_lds_dwordx4 v[140:141], off
	v_lshl_add_u64 v[140:141], v[218:219], 0, s[36:37]
	s_add_i32 m0, s51, 0x2000
	s_nop 0
	global_load_lds_dwordx4 v[140:141], off
	s_barrier
	s_waitcnt lgkmcnt(0)
	s_waitcnt lgkmcnt(0)
	v_mfma_f32_16x16x32_bf16 v[118:121], v[194:197], v[162:165], v[118:121]
	v_mfma_f32_16x16x32_bf16 v[110:113], v[202:205], v[162:165], v[110:113]
	v_mfma_f32_16x16x32_bf16 v[102:105], v[194:197], v[170:173], v[102:105]
	v_mfma_f32_16x16x32_bf16 v[94:97], v[202:205], v[170:173], v[94:97]
	v_mfma_f32_16x16x32_bf16 v[86:89], v[194:197], v[178:181], v[86:89]
	v_mfma_f32_16x16x32_bf16 v[78:81], v[202:205], v[178:181], v[78:81]
	v_mfma_f32_16x16x32_bf16 v[70:73], v[194:197], v[186:189], v[70:73]
	v_mfma_f32_16x16x32_bf16 v[66:69], v[202:205], v[186:189], v[66:69]
	v_mfma_f32_16x16x32_bf16 v[118:121], v[198:201], v[166:169], v[118:121]
	v_mfma_f32_16x16x32_bf16 v[110:113], v[234:237], v[166:169], v[110:113]
	v_mfma_f32_16x16x32_bf16 v[102:105], v[198:201], v[174:177], v[102:105]
	v_mfma_f32_16x16x32_bf16 v[94:97], v[234:237], v[174:177], v[94:97]
	v_mfma_f32_16x16x32_bf16 v[86:89], v[198:201], v[182:185], v[86:89]
	v_mfma_f32_16x16x32_bf16 v[78:81], v[234:237], v[182:185], v[78:81]
	v_mfma_f32_16x16x32_bf16 v[70:73], v[198:201], v[190:193], v[70:73]
	v_mfma_f32_16x16x32_bf16 v[66:69], v[234:237], v[190:193], v[66:69]
	s_mov_b32 m0, s33
	v_lshl_add_u64 v[140:141], v[238:239], 0, s[36:37]
	s_barrier
	ds_read_b128 v[162:165], v145 offset:49152
	ds_read_b128 v[166:169], v145 offset:50176
	ds_read_b128 v[170:173], v145 offset:51200
	ds_read_b128 v[174:177], v145 offset:52224
	ds_read_b128 v[178:181], v145 offset:53248
	ds_read_b128 v[182:185], v145 offset:54272
	ds_read_b128 v[186:189], v145 offset:55296
	ds_read_b128 v[190:193], v145 offset:56320
	global_load_lds_dwordx4 v[140:141], off
	v_lshl_add_u64 v[140:141], v[240:241], 0, s[36:37]
	s_mov_b32 m0, s46
	s_nop 0
	global_load_lds_dwordx4 v[140:141], off
	s_barrier
	s_waitcnt lgkmcnt(0)
	s_waitcnt lgkmcnt(0)
	v_mfma_f32_16x16x32_bf16 v[62:65], v[146:149], v[162:165], v[62:65]
	v_mfma_f32_16x16x32_bf16 v[58:61], v[154:157], v[162:165], v[58:61]
	v_mfma_f32_16x16x32_bf16 v[50:53], v[146:149], v[170:173], v[50:53]
	v_mfma_f32_16x16x32_bf16 v[42:45], v[154:157], v[170:173], v[42:45]
	v_mfma_f32_16x16x32_bf16 v[34:37], v[146:149], v[178:181], v[34:37]
	v_mfma_f32_16x16x32_bf16 v[26:29], v[154:157], v[178:181], v[26:29]
	v_mfma_f32_16x16x32_bf16 v[18:21], v[146:149], v[186:189], v[18:21]
	v_mfma_f32_16x16x32_bf16 v[10:13], v[154:157], v[186:189], v[10:13]
	v_mfma_f32_16x16x32_bf16 v[62:65], v[150:153], v[166:169], v[62:65]
	v_mfma_f32_16x16x32_bf16 v[58:61], v[158:161], v[166:169], v[58:61]
	v_mfma_f32_16x16x32_bf16 v[50:53], v[150:153], v[174:177], v[50:53]
	v_mfma_f32_16x16x32_bf16 v[42:45], v[158:161], v[174:177], v[42:45]
	v_mfma_f32_16x16x32_bf16 v[34:37], v[150:153], v[182:185], v[34:37]
	v_mfma_f32_16x16x32_bf16 v[26:29], v[158:161], v[182:185], v[26:29]
	v_mfma_f32_16x16x32_bf16 v[18:21], v[150:153], v[190:193], v[18:21]
	v_mfma_f32_16x16x32_bf16 v[10:13], v[158:161], v[190:193], v[10:13]
	s_barrier
	s_add_u32 s42, s42, 0x80080
	s_addc_u32 s43, s43, 0
	s_add_i32 s50, s50, s7
	v_lshl_add_u64 v[140:141], s[42:43], 0, v[210:211]
	s_mov_b32 m0, s50
	s_nop 0
	global_load_lds_dwordx4 v[140:141], off
	v_lshl_add_u64 v[140:141], s[42:43], 0, v[130:131]
	s_add_i32 m0, s50, 0x2000
	s_nop 0
	global_load_lds_dwordx4 v[140:141], off
	s_waitcnt vmcnt(6)
	s_barrier
	v_mfma_f32_16x16x32_bf16 v[54:57], v[194:197], v[162:165], v[54:57]
	v_mfma_f32_16x16x32_bf16 v[46:49], v[202:205], v[162:165], v[46:49]
	v_mfma_f32_16x16x32_bf16 v[38:41], v[194:197], v[170:173], v[38:41]
	v_mfma_f32_16x16x32_bf16 v[30:33], v[202:205], v[170:173], v[30:33]
	v_mfma_f32_16x16x32_bf16 v[22:25], v[194:197], v[178:181], v[22:25]
	v_mfma_f32_16x16x32_bf16 v[14:17], v[202:205], v[178:181], v[14:17]
	v_mfma_f32_16x16x32_bf16 v[6:9], v[194:197], v[186:189], v[6:9]
	v_mfma_f32_16x16x32_bf16 v[2:5], v[202:205], v[186:189], v[2:5]
	v_mfma_f32_16x16x32_bf16 v[54:57], v[198:201], v[166:169], v[54:57]
	v_mfma_f32_16x16x32_bf16 v[46:49], v[234:237], v[166:169], v[46:49]
	v_mfma_f32_16x16x32_bf16 v[38:41], v[198:201], v[174:177], v[38:41]
	v_mfma_f32_16x16x32_bf16 v[30:33], v[234:237], v[174:177], v[30:33]
	v_mfma_f32_16x16x32_bf16 v[22:25], v[198:201], v[182:185], v[22:25]
	v_mfma_f32_16x16x32_bf16 v[14:17], v[234:237], v[182:185], v[14:17]
	v_mfma_f32_16x16x32_bf16 v[6:9], v[198:201], v[190:193], v[6:9]
	v_mfma_f32_16x16x32_bf16 v[2:5], v[234:237], v[190:193], v[2:5]
	s_add_i32 s61, s61, 2
	s_add_u32 s40, s40, 0x100
	s_addc_u32 s41, s41, 0
	s_add_u32 s58, s58, 0x100
	s_addc_u32 s60, s60, 0
	s_cmp_gt_u32 s61, 29
	s_barrier
	s_cbranch_scc0 .LBB0_169
	v_lshl_or_b32 v140, s4, 8, v144
	v_ashrrev_i32_e32 v141, 31, v140
	v_lshl_add_u32 v150, s5, 8, v142
	v_lshl_add_u64 v[140:141], v[140:141], 1, s[8:9]
	s_movk_i32 s58, 0x2c00
	v_mad_i64_i32 v[146:147], s[4:5], v150, s58, v[140:141]
	v_pk_add_f32 v[128:129], v[128:129], 0 op_sel_hi:[1,0]
	v_pk_add_f32 v[126:127], v[126:127], 0 op_sel_hi:[1,0]
	v_pk_add_f32 v[148:149], v[124:125], 0 op_sel_hi:[1,0]
	v_pk_add_f32 v[124:125], v[122:123], 0 op_sel_hi:[1,0]
	v_cvt_pk_bf16_f32 v122, v126, v127
	v_cvt_pk_bf16_f32 v123, v128, v129
	v_pk_add_f32 v[118:119], v[118:119], 0 op_sel_hi:[1,0]
	v_cvt_pk_bf16_f32 v124, v124, v125
	v_cvt_pk_bf16_f32 v125, v148, v149
	global_store_dwordx4 v[146:147], v[122:125], off
	v_pk_add_f32 v[120:121], v[120:121], 0 op_sel_hi:[1,0]
	v_pk_add_f32 v[114:115], v[114:115], 0 op_sel_hi:[1,0]
	v_pk_add_f32 v[122:123], v[112:113], 0 op_sel_hi:[1,0]
	v_pk_add_f32 v[112:113], v[110:111], 0 op_sel_hi:[1,0]
	v_cvt_pk_bf16_f32 v110, v118, v119
	v_cvt_pk_bf16_f32 v111, v120, v121
	v_pk_add_f32 v[102:103], v[102:103], 0 op_sel_hi:[1,0]
	v_cvt_pk_bf16_f32 v112, v112, v113
	v_cvt_pk_bf16_f32 v113, v122, v123
	global_store_dwordx4 v[146:147], v[110:113], off offset:256
	v_pk_add_f32 v[104:105], v[104:105], 0 op_sel_hi:[1,0]
	v_pk_add_f32 v[98:99], v[98:99], 0 op_sel_hi:[1,0]
	v_or_b32_e32 v110, 16, v150
	v_mad_i64_i32 v[110:111], s[4:5], v110, s58, v[140:141]
	v_pk_add_f32 v[112:113], v[116:117], 0 op_sel_hi:[1,0]
	v_pk_add_f32 v[116:117], v[108:109], 0 op_sel_hi:[1,0]
	v_pk_add_f32 v[108:109], v[106:107], 0 op_sel_hi:[1,0]
	v_cvt_pk_bf16_f32 v106, v114, v115
	v_cvt_pk_bf16_f32 v107, v112, v113
	v_pk_add_f32 v[86:87], v[86:87], 0 op_sel_hi:[1,0]
	v_cvt_pk_bf16_f32 v108, v108, v109
	v_cvt_pk_bf16_f32 v109, v116, v117
	global_store_dwordx4 v[110:111], v[106:109], off
	v_pk_add_f32 v[88:89], v[88:89], 0 op_sel_hi:[1,0]
	v_pk_add_f32 v[82:83], v[82:83], 0 op_sel_hi:[1,0]
	v_pk_add_f32 v[106:107], v[96:97], 0 op_sel_hi:[1,0]
	v_pk_add_f32 v[96:97], v[94:95], 0 op_sel_hi:[1,0]
	v_cvt_pk_bf16_f32 v94, v102, v103
	v_cvt_pk_bf16_f32 v95, v104, v105
	v_pk_add_f32 v[70:71], v[70:71], 0 op_sel_hi:[1,0]
	v_cvt_pk_bf16_f32 v96, v96, v97
	v_cvt_pk_bf16_f32 v97, v106, v107
	global_store_dwordx4 v[110:111], v[94:97], off offset:256
	v_pk_add_f32 v[72:73], v[72:73], 0 op_sel_hi:[1,0]
	v_pk_add_f32 v[64:65], v[64:65], 0 op_sel_hi:[1,0]
	v_or_b32_e32 v94, 32, v150
	v_mad_i64_i32 v[94:95], s[4:5], v94, s58, v[140:141]
	v_pk_add_f32 v[96:97], v[100:101], 0 op_sel_hi:[1,0]
	v_pk_add_f32 v[100:101], v[92:93], 0 op_sel_hi:[1,0]
	v_pk_add_f32 v[92:93], v[90:91], 0 op_sel_hi:[1,0]
	v_cvt_pk_bf16_f32 v90, v98, v99
	v_cvt_pk_bf16_f32 v91, v96, v97
	v_pk_add_f32 v[62:63], v[62:63], 0 op_sel_hi:[1,0]
	v_cvt_pk_bf16_f32 v92, v92, v93
	v_cvt_pk_bf16_f32 v93, v100, v101
	global_store_dwordx4 v[94:95], v[90:93], off
	v_pk_add_f32 v[54:55], v[54:55], 0 op_sel_hi:[1,0]
	v_pk_add_f32 v[56:57], v[56:57], 0 op_sel_hi:[1,0]
	v_pk_add_f32 v[90:91], v[80:81], 0 op_sel_hi:[1,0]
	v_pk_add_f32 v[80:81], v[78:79], 0 op_sel_hi:[1,0]
	v_cvt_pk_bf16_f32 v78, v86, v87
	v_cvt_pk_bf16_f32 v79, v88, v89
	v_pk_add_f32 v[50:51], v[50:51], 0 op_sel_hi:[1,0]
	v_cvt_pk_bf16_f32 v80, v80, v81
	v_cvt_pk_bf16_f32 v81, v90, v91
	global_store_dwordx4 v[94:95], v[78:81], off offset:256
	v_pk_add_f32 v[38:39], v[38:39], 0 op_sel_hi:[1,0]
	v_pk_add_f32 v[40:41], v[40:41], 0 op_sel_hi:[1,0]
	v_or_b32_e32 v78, 48, v150
	v_mad_i64_i32 v[78:79], s[4:5], v78, s58, v[140:141]
	v_pk_add_f32 v[80:81], v[84:85], 0 op_sel_hi:[1,0]
	v_pk_add_f32 v[84:85], v[76:77], 0 op_sel_hi:[1,0]
	v_pk_add_f32 v[76:77], v[74:75], 0 op_sel_hi:[1,0]
	v_cvt_pk_bf16_f32 v74, v82, v83
	v_cvt_pk_bf16_f32 v75, v80, v81
	v_pk_add_f32 v[34:35], v[34:35], 0 op_sel_hi:[1,0]
	v_cvt_pk_bf16_f32 v76, v76, v77
	v_cvt_pk_bf16_f32 v77, v84, v85
	global_store_dwordx4 v[78:79], v[74:77], off
	v_pk_add_f32 v[22:23], v[22:23], 0 op_sel_hi:[1,0]
	v_pk_add_f32 v[24:25], v[24:25], 0 op_sel_hi:[1,0]
	v_pk_add_f32 v[74:75], v[68:69], 0 op_sel_hi:[1,0]
	v_pk_add_f32 v[68:69], v[66:67], 0 op_sel_hi:[1,0]
	v_cvt_pk_bf16_f32 v66, v70, v71
	v_cvt_pk_bf16_f32 v67, v72, v73
	v_pk_add_f32 v[18:19], v[18:19], 0 op_sel_hi:[1,0]
	v_cvt_pk_bf16_f32 v68, v68, v69
	v_cvt_pk_bf16_f32 v69, v74, v75
	global_store_dwordx4 v[78:79], v[66:69], off offset:256
	v_readlane_b32 s64, v255, 43
	v_readlane_b32 s60, v255, 45
	v_add_u32_e32 v66, 0x80, v150
	v_mad_i64_i32 v[66:67], s[4:5], v66, s58, v[140:141]
	v_pk_add_f32 v[68:69], v[60:61], 0 op_sel_hi:[1,0]
	v_pk_add_f32 v[60:61], v[58:59], 0 op_sel_hi:[1,0]
	v_cvt_pk_bf16_f32 v58, v62, v63
	v_cvt_pk_bf16_f32 v59, v64, v65
	s_and_b64 vcc, exec, s[38:39]
	v_cvt_pk_bf16_f32 v60, v60, v61
	v_cvt_pk_bf16_f32 v61, v68, v69
	global_store_dwordx4 v[66:67], v[58:61], off
	s_mov_b64 s[42:43], s[34:35]
	s_mov_b64 s[40:41], s[24:25]
	v_pk_add_f32 v[58:59], v[48:49], 0 op_sel_hi:[1,0]
	v_pk_add_f32 v[48:49], v[46:47], 0 op_sel_hi:[1,0]
	v_cvt_pk_bf16_f32 v46, v54, v55
	v_cvt_pk_bf16_f32 v47, v56, v57
	v_readlane_b32 s65, v255, 44
	v_cvt_pk_bf16_f32 v48, v48, v49
	v_cvt_pk_bf16_f32 v49, v58, v59
	global_store_dwordx4 v[66:67], v[46:49], off offset:256
	v_readlane_b32 s61, v255, 46
	v_pk_add_f32 v[8:9], v[8:9], 0 op_sel_hi:[1,0]
	v_add_u32_e32 v46, 0x90, v150
	v_mad_i64_i32 v[46:47], s[4:5], v46, s58, v[140:141]
	v_pk_add_f32 v[48:49], v[52:53], 0 op_sel_hi:[1,0]
	v_pk_add_f32 v[52:53], v[44:45], 0 op_sel_hi:[1,0]
	v_pk_add_f32 v[44:45], v[42:43], 0 op_sel_hi:[1,0]
	v_cvt_pk_bf16_f32 v42, v50, v51
	v_cvt_pk_bf16_f32 v43, v48, v49
	v_pk_add_f32 v[6:7], v[6:7], 0 op_sel_hi:[1,0]
	v_cvt_pk_bf16_f32 v44, v44, v45
	v_cvt_pk_bf16_f32 v45, v52, v53
	global_store_dwordx4 v[46:47], v[42:45], off
	s_nop 1
	v_pk_add_f32 v[42:43], v[32:33], 0 op_sel_hi:[1,0]
	v_pk_add_f32 v[32:33], v[30:31], 0 op_sel_hi:[1,0]
	v_cvt_pk_bf16_f32 v30, v38, v39
	v_cvt_pk_bf16_f32 v31, v40, v41
	s_nop 0
	v_cvt_pk_bf16_f32 v32, v32, v33
	v_cvt_pk_bf16_f32 v33, v42, v43
	global_store_dwordx4 v[46:47], v[30:33], off offset:256
	s_nop 1
	v_add_u32_e32 v30, 0xa0, v150
	v_mad_i64_i32 v[30:31], s[4:5], v30, s58, v[140:141]
	v_pk_add_f32 v[32:33], v[36:37], 0 op_sel_hi:[1,0]
	v_pk_add_f32 v[36:37], v[28:29], 0 op_sel_hi:[1,0]
	v_pk_add_f32 v[28:29], v[26:27], 0 op_sel_hi:[1,0]
	v_cvt_pk_bf16_f32 v26, v34, v35
	v_cvt_pk_bf16_f32 v27, v32, v33
	s_nop 0
	v_cvt_pk_bf16_f32 v28, v28, v29
	v_cvt_pk_bf16_f32 v29, v36, v37
	global_store_dwordx4 v[30:31], v[26:29], off
	s_nop 1
	v_pk_add_f32 v[26:27], v[16:17], 0 op_sel_hi:[1,0]
	v_pk_add_f32 v[16:17], v[14:15], 0 op_sel_hi:[1,0]
	v_cvt_pk_bf16_f32 v14, v22, v23
	v_cvt_pk_bf16_f32 v15, v24, v25
	s_nop 0
	v_cvt_pk_bf16_f32 v16, v16, v17
	v_cvt_pk_bf16_f32 v17, v26, v27
	global_store_dwordx4 v[30:31], v[14:17], off offset:256
	s_nop 1
	v_add_u32_e32 v14, 0xb0, v150
	v_mad_i64_i32 v[14:15], s[4:5], v14, s58, v[140:141]
	v_pk_add_f32 v[16:17], v[20:21], 0 op_sel_hi:[1,0]
	v_pk_add_f32 v[20:21], v[12:13], 0 op_sel_hi:[1,0]
	v_pk_add_f32 v[12:13], v[10:11], 0 op_sel_hi:[1,0]
	v_cvt_pk_bf16_f32 v10, v18, v19
	v_cvt_pk_bf16_f32 v11, v16, v17
	s_mov_b32 s4, s0
	v_cvt_pk_bf16_f32 v12, v12, v13
	v_cvt_pk_bf16_f32 v13, v20, v21
	global_store_dwordx4 v[14:15], v[10:13], off
	s_mov_b32 s5, s10
	s_nop 0
	v_pk_add_f32 v[10:11], v[4:5], 0 op_sel_hi:[1,0]
	v_pk_add_f32 v[4:5], v[2:3], 0 op_sel_hi:[1,0]
	v_cvt_pk_bf16_f32 v2, v6, v7
	v_cvt_pk_bf16_f32 v3, v8, v9
	s_nop 0
	v_cvt_pk_bf16_f32 v4, v4, v5
	v_cvt_pk_bf16_f32 v5, v10, v11
	global_store_dwordx4 v[14:15], v[2:5], off offset:256
	s_cbranch_vccz .LBB0_162
	s_waitcnt vmcnt(0)
	v_readlane_b32 s46, v255, 41
	s_cmpk_gt_u32 s2, 0xff
	v_readlane_b32 s47, v255, 42
	s_cbranch_scc1 .LBB0_173
	s_barrier

.LBB0_174:
	s_setprio 0
	s_waitcnt vmcnt(0)
	s_waitcnt vmcnt(0) lgkmcnt(0)
	s_barrier
	s_and_saveexec_b64 s[0:1], s[44:45]
	s_cbranch_execz .LBB0_222
	v_readlane_b32 s2, v255, 29
	s_waitcnt vmcnt(0) expcnt(0) lgkmcnt(0)
	s_nop 0
	v_mov_b32_e32 v2, s2
	ds_read_b32 v4, v2
	v_readlane_b32 s2, v255, 30
	s_waitcnt lgkmcnt(0)
	v_cmp_ne_u32_e32 vcc, 0, v4
	v_mov_b32_e32 v2, s2
	ds_read_b32 v2, v2
	s_cbranch_vccnz .LBB0_190
	v_readlane_b32 s4, v253, 16
	v_readlane_b32 s5, v253, 17
	s_load_dwordx2 s[2:3], s[4:5], 0x4
	s_waitcnt lgkmcnt(0)
	s_mul_i32 s2, s2, s86
	s_mul_i32 s2, s2, s3
	s_mov_b32 s3, 1
	s_branch .LBB0_178

.LBB0_477:
	v_lshl_or_b32 v168, s34, 8, v171
	v_ashrrev_i32_e32 v169, 31, v168
	v_lshl_add_u64 v[130:131], v[168:169], 2, s[62:63]
	global_load_dwordx4 v[142:145], v[130:131], off
	global_load_dwordx4 v[138:141], v[130:131], off offset:64
	global_load_dwordx4 v[134:137], v[130:131], off offset:512
	s_nop 0
	global_load_dwordx4 v[130:133], v[130:131], off offset:576
	v_lshl_add_u64 v[250:251], v[148:149], 0, v[168:169]
	v_lshlrev_b64 v[250:251], 2, v[250:251]
	v_lshl_add_u64 v[218:219], s[0:1], 0, v[250:251]
	global_load_dwordx4 v[174:177], v[218:219], off
	global_load_dwordx4 v[178:181], v[218:219], off offset:64
	global_load_dwordx4 v[182:185], v[218:219], off offset:512
	global_load_dwordx4 v[186:189], v[218:219], off offset:576
	v_lshl_add_u64 v[250:251], v[150:151], 0, v[168:169]
	v_lshlrev_b64 v[250:251], 2, v[250:251]
	v_lshl_add_u64 v[218:219], s[0:1], 0, v[250:251]
	global_load_dwordx4 v[190:193], v[218:219], off
	global_load_dwordx4 v[194:197], v[218:219], off offset:64
	global_load_dwordx4 v[198:201], v[218:219], off offset:512
	global_load_dwordx4 v[202:205], v[218:219], off offset:576
	v_lshl_add_u64 v[250:251], v[152:153], 0, v[168:169]
	v_lshlrev_b64 v[250:251], 2, v[250:251]
	v_lshl_add_u64 v[218:219], s[0:1], 0, v[250:251]
	global_load_dwordx4 v[234:237], v[218:219], off
	global_load_dwordx4 v[238:241], v[218:219], off offset:64
	global_load_dwordx4 v[242:245], v[218:219], off offset:512
	global_load_dwordx4 v[246:249], v[218:219], off offset:576
	s_and_b64 vcc, exec, s[38:39]
	s_mov_b32 s34, s24
	s_mov_b32 s74, s40
	s_mov_b64 s[76:77], s[42:43]
	s_waitcnt vmcnt(8)
	v_lshl_add_u64 v[250:251], v[148:149], 0, v[168:169]
	v_lshlrev_b64 v[250:251], 2, v[250:251]
	v_lshl_add_u64 v[226:227], s[50:51], 0, v[250:251]
	v_pk_fma_f32 v[128:129], v[128:129], v[144:145], v[176:177]
	v_pk_fma_f32 v[126:127], v[126:127], v[142:143], v[174:175]
	v_pk_fma_f32 v[124:125], v[124:125], v[140:141], v[180:181]
	v_pk_fma_f32 v[122:123], v[122:123], v[138:139], v[178:179]
	v_pk_fma_f32 v[120:121], v[120:121], v[136:137], v[184:185]
	v_pk_fma_f32 v[118:119], v[118:119], v[134:135], v[182:183]
	v_pk_fma_f32 v[108:109], v[108:109], v[132:133], v[188:189]
	v_pk_fma_f32 v[106:107], v[106:107], v[130:131], v[186:187]
	global_store_dwordx4 v[226:227], v[126:129], off
	global_store_dwordx4 v[226:227], v[122:125], off offset:64
	global_store_dwordx4 v[226:227], v[118:121], off offset:512
	global_store_dwordx4 v[226:227], v[106:109], off offset:576
	v_lshl_add_u64 v[250:251], v[154:155], 0, v[168:169]
	v_lshlrev_b64 v[250:251], 2, v[250:251]
	v_lshl_add_u64 v[218:219], s[0:1], 0, v[250:251]
	global_load_dwordx4 v[174:177], v[218:219], off
	global_load_dwordx4 v[178:181], v[218:219], off offset:64
	global_load_dwordx4 v[182:185], v[218:219], off offset:512
	global_load_dwordx4 v[186:189], v[218:219], off offset:576
	s_waitcnt vmcnt(12)
	v_lshl_add_u64 v[250:251], v[150:151], 0, v[168:169]
	v_lshlrev_b64 v[250:251], 2, v[250:251]
	v_lshl_add_u64 v[226:227], s[50:51], 0, v[250:251]
	v_pk_fma_f32 v[116:117], v[116:117], v[144:145], v[192:193]
	v_pk_fma_f32 v[114:115], v[114:115], v[142:143], v[190:191]
	v_pk_fma_f32 v[112:113], v[112:113], v[140:141], v[196:197]
	v_pk_fma_f32 v[110:111], v[110:111], v[138:139], v[194:195]
	v_pk_fma_f32 v[104:105], v[104:105], v[136:137], v[200:201]
	v_pk_fma_f32 v[102:103], v[102:103], v[134:135], v[198:199]
	v_pk_fma_f32 v[92:93], v[92:93], v[132:133], v[204:205]
	v_pk_fma_f32 v[90:91], v[90:91], v[130:131], v[202:203]
	global_store_dwordx4 v[226:227], v[114:117], off
	global_store_dwordx4 v[226:227], v[110:113], off offset:64
	global_store_dwordx4 v[226:227], v[102:105], off offset:512
	global_store_dwordx4 v[226:227], v[90:93], off offset:576
	v_lshl_add_u64 v[250:251], v[156:157], 0, v[168:169]
	v_lshlrev_b64 v[250:251], 2, v[250:251]
	v_lshl_add_u64 v[218:219], s[0:1], 0, v[250:251]
	global_load_dwordx4 v[190:193], v[218:219], off
	global_load_dwordx4 v[194:197], v[218:219], off offset:64
	global_load_dwordx4 v[198:201], v[218:219], off offset:512
	global_load_dwordx4 v[202:205], v[218:219], off offset:576
	s_waitcnt vmcnt(16)
	v_lshl_add_u64 v[250:251], v[152:153], 0, v[168:169]
	v_lshlrev_b64 v[250:251], 2, v[250:251]
	v_lshl_add_u64 v[226:227], s[50:51], 0, v[250:251]
	v_pk_fma_f32 v[100:101], v[100:101], v[144:145], v[236:237]
	v_pk_fma_f32 v[98:99], v[98:99], v[142:143], v[234:235]
	v_pk_fma_f32 v[96:97], v[96:97], v[140:141], v[240:241]
	v_pk_fma_f32 v[94:95], v[94:95], v[138:139], v[238:239]
	v_pk_fma_f32 v[88:89], v[88:89], v[136:137], v[244:245]
	v_pk_fma_f32 v[86:87], v[86:87], v[134:135], v[242:243]
	v_pk_fma_f32 v[76:77], v[76:77], v[132:133], v[248:249]
	v_pk_fma_f32 v[74:75], v[74:75], v[130:131], v[246:247]
	global_store_dwordx4 v[226:227], v[98:101], off
	global_store_dwordx4 v[226:227], v[94:97], off offset:64
	global_store_dwordx4 v[226:227], v[86:89], off offset:512
	global_store_dwordx4 v[226:227], v[74:77], off offset:576
	v_lshl_add_u64 v[250:251], v[158:159], 0, v[168:169]
	v_lshlrev_b64 v[250:251], 2, v[250:251]
	v_lshl_add_u64 v[218:219], s[0:1], 0, v[250:251]
	global_load_dwordx4 v[234:237], v[218:219], off
	global_load_dwordx4 v[238:241], v[218:219], off offset:64
	global_load_dwordx4 v[242:245], v[218:219], off offset:512
	global_load_dwordx4 v[246:249], v[218:219], off offset:576
	s_waitcnt vmcnt(16)
	v_lshl_add_u64 v[250:251], v[154:155], 0, v[168:169]
	v_lshlrev_b64 v[250:251], 2, v[250:251]
	v_lshl_add_u64 v[226:227], s[50:51], 0, v[250:251]
	v_pk_fma_f32 v[84:85], v[84:85], v[144:145], v[176:177]
	v_pk_fma_f32 v[82:83], v[82:83], v[142:143], v[174:175]
	v_pk_fma_f32 v[80:81], v[80:81], v[140:141], v[180:181]
	v_pk_fma_f32 v[78:79], v[78:79], v[138:139], v[178:179]
	v_pk_fma_f32 v[72:73], v[72:73], v[136:137], v[184:185]
	v_pk_fma_f32 v[70:71], v[70:71], v[134:135], v[182:183]
	v_pk_fma_f32 v[68:69], v[68:69], v[132:133], v[188:189]
	v_pk_fma_f32 v[66:67], v[66:67], v[130:131], v[186:187]
	global_store_dwordx4 v[226:227], v[82:85], off
	global_store_dwordx4 v[226:227], v[78:81], off offset:64
	global_store_dwordx4 v[226:227], v[70:73], off offset:512
	global_store_dwordx4 v[226:227], v[66:69], off offset:576
	v_lshl_add_u64 v[250:251], v[160:161], 0, v[168:169]
	v_lshlrev_b64 v[250:251], 2, v[250:251]
	v_lshl_add_u64 v[218:219], s[0:1], 0, v[250:251]
	global_load_dwordx4 v[174:177], v[218:219], off
	global_load_dwordx4 v[178:181], v[218:219], off offset:64
	global_load_dwordx4 v[182:185], v[218:219], off offset:512
	global_load_dwordx4 v[186:189], v[218:219], off offset:576
	s_waitcnt vmcnt(16)
	v_lshl_add_u64 v[250:251], v[156:157], 0, v[168:169]
	v_lshlrev_b64 v[250:251], 2, v[250:251]
	v_lshl_add_u64 v[226:227], s[50:51], 0, v[250:251]
	v_pk_fma_f32 v[64:65], v[64:65], v[144:145], v[192:193]
	v_pk_fma_f32 v[62:63], v[62:63], v[142:143], v[190:191]
	v_pk_fma_f32 v[60:61], v[60:61], v[140:141], v[196:197]
	v_pk_fma_f32 v[58:59], v[58:59], v[138:139], v[194:195]
	v_pk_fma_f32 v[56:57], v[56:57], v[136:137], v[200:201]
	v_pk_fma_f32 v[54:55], v[54:55], v[134:135], v[198:199]
	v_pk_fma_f32 v[44:45], v[44:45], v[132:133], v[204:205]
	v_pk_fma_f32 v[42:43], v[42:43], v[130:131], v[202:203]
	global_store_dwordx4 v[226:227], v[62:65], off
	global_store_dwordx4 v[226:227], v[58:61], off offset:64
	global_store_dwordx4 v[226:227], v[54:57], off offset:512
	global_store_dwordx4 v[226:227], v[42:45], off offset:576
	v_lshl_add_u64 v[250:251], v[162:163], 0, v[168:169]
	v_lshlrev_b64 v[250:251], 2, v[250:251]
	v_lshl_add_u64 v[218:219], s[0:1], 0, v[250:251]
	global_load_dwordx4 v[190:193], v[218:219], off
	global_load_dwordx4 v[194:197], v[218:219], off offset:64
	global_load_dwordx4 v[198:201], v[218:219], off offset:512
	global_load_dwordx4 v[202:205], v[218:219], off offset:576
	s_waitcnt vmcnt(16)
	v_lshl_add_u64 v[250:251], v[158:159], 0, v[168:169]
	v_lshlrev_b64 v[250:251], 2, v[250:251]
	v_lshl_add_u64 v[226:227], s[50:51], 0, v[250:251]
	v_pk_fma_f32 v[52:53], v[52:53], v[144:145], v[236:237]
	v_pk_fma_f32 v[50:51], v[50:51], v[142:143], v[234:235]
	v_pk_fma_f32 v[48:49], v[48:49], v[140:141], v[240:241]
	v_pk_fma_f32 v[46:47], v[46:47], v[138:139], v[238:239]
	v_pk_fma_f32 v[40:41], v[40:41], v[136:137], v[244:245]
	v_pk_fma_f32 v[38:39], v[38:39], v[134:135], v[242:243]
	v_pk_fma_f32 v[28:29], v[28:29], v[132:133], v[248:249]
	v_pk_fma_f32 v[26:27], v[26:27], v[130:131], v[246:247]
	global_store_dwordx4 v[226:227], v[50:53], off
	global_store_dwordx4 v[226:227], v[46:49], off offset:64
	global_store_dwordx4 v[226:227], v[38:41], off offset:512
	global_store_dwordx4 v[226:227], v[26:29], off offset:576
	s_waitcnt vmcnt(12)
	v_lshl_add_u64 v[250:251], v[160:161], 0, v[168:169]
	v_lshlrev_b64 v[250:251], 2, v[250:251]
	v_lshl_add_u64 v[226:227], s[50:51], 0, v[250:251]
	v_pk_fma_f32 v[36:37], v[36:37], v[144:145], v[176:177]
	v_pk_fma_f32 v[34:35], v[34:35], v[142:143], v[174:175]
	v_pk_fma_f32 v[32:33], v[32:33], v[140:141], v[180:181]
	v_pk_fma_f32 v[30:31], v[30:31], v[138:139], v[178:179]
	v_pk_fma_f32 v[24:25], v[24:25], v[136:137], v[184:185]
	v_pk_fma_f32 v[22:23], v[22:23], v[134:135], v[182:183]
	v_pk_fma_f32 v[12:13], v[12:13], v[132:133], v[188:189]
	v_pk_fma_f32 v[10:11], v[10:11], v[130:131], v[186:187]
	global_store_dwordx4 v[226:227], v[34:37], off
	global_store_dwordx4 v[226:227], v[30:33], off offset:64
	global_store_dwordx4 v[226:227], v[22:25], off offset:512
	global_store_dwordx4 v[226:227], v[10:13], off offset:576
	s_waitcnt vmcnt(8)
	v_lshl_add_u64 v[250:251], v[162:163], 0, v[168:169]
	v_lshlrev_b64 v[250:251], 2, v[250:251]
	v_lshl_add_u64 v[226:227], s[50:51], 0, v[250:251]
	v_pk_fma_f32 v[20:21], v[20:21], v[144:145], v[192:193]
	v_pk_fma_f32 v[18:19], v[18:19], v[142:143], v[190:191]
	v_pk_fma_f32 v[16:17], v[16:17], v[140:141], v[196:197]
	v_pk_fma_f32 v[14:15], v[14:15], v[138:139], v[194:195]
	v_pk_fma_f32 v[8:9], v[8:9], v[136:137], v[200:201]
	v_pk_fma_f32 v[6:7], v[6:7], v[134:135], v[198:199]
	v_pk_fma_f32 v[4:5], v[4:5], v[132:133], v[204:205]
	v_pk_fma_f32 v[2:3], v[2:3], v[130:131], v[202:203]
	global_store_dwordx4 v[226:227], v[18:21], off
	global_store_dwordx4 v[226:227], v[14:17], off offset:64
	global_store_dwordx4 v[226:227], v[6:9], off offset:512
	global_store_dwordx4 v[226:227], v[2:5], off offset:576
	s_mov_b64 s[50:51], s[86:87]
	v_readlane_b32 s86, v255, 33
	v_readlane_b32 s87, v255, 34
	s_cbranch_vccnz .LBB0_486
.LBB0_478:
	v_readfirstlane_b32 s98, v0
	s_nop 3
	s_cmp_ge_u32 s98, 0x100
	s_cbranch_scc0 .Lgp_g6
	s_setprio 1
.Lgp_g6:
	s_add_i32 s29, s29, 1
	s_mul_i32 s0, s29, s87
	s_mul_hi_u32 s1, s29, s86
	s_add_i32 s1, s1, s0
	s_mul_i32 s0, s29, s86
	s_add_u32 s42, s0, s70
	s_addc_u32 s43, s1, s71
	v_mov_b64_e32 v[2:3], s[80:81]
	v_cmp_ge_i64_e64 s[38:39], s[42:43], v[2:3]
	v_cmp_lt_i64_e64 s[0:1], s[42:43], v[2:3]
	s_and_b64 vcc, exec, s[38:39]
	s_cbranch_vccnz .LBB0_480
	s_ashr_i32 s4, s42, 31
	s_lshr_b32 s4, s4, 29
	s_add_i32 s4, s42, s4
	s_ashr_i32 s5, s4, 3
	s_and_b32 s4, s4, -8
	s_sub_i32 s4, s42, s4
	s_cmp_lt_i32 s4, 0
	s_cselect_b32 s24, s47, s84
	s_mul_i32 s4, s24, s4
	s_add_i32 s4, s4, s5
	s_ashr_i32 s5, s4, 31
	s_lshr_b32 s5, s5, 26
	s_add_i32 s5, s4, s5
	s_ashr_i32 s24, s5, 6
	s_lshl_b32 s25, s24, 3
	s_sub_i32 s24, s84, s25
	s_min_i32 s40, s24, 8
	s_abs_i32 s24, s40
	v_cvt_f32_u32_e32 v2, s24
	s_sub_i32 s42, 0, s24
	s_andn2_b32 s5, s5, 63
	s_sub_i32 s4, s4, s5
	v_rcp_iflag_f32_e32 v2, v2
	s_abs_i32 s5, s4
	s_xor_b32 s41, s4, s40
	s_ashr_i32 s41, s41, 31
	v_mul_f32_e32 v2, 0x4f7ffffe, v2
	v_cvt_u32_f32_e32 v2, v2
	s_nop 0
	v_readfirstlane_b32 s43, v2
	s_mul_i32 s42, s42, s43
	s_mul_hi_u32 s42, s43, s42
	s_add_i32 s43, s43, s42
	s_mul_hi_u32 s42, s5, s43
	s_mul_i32 s43, s42, s24
	s_sub_i32 s5, s5, s43
	s_add_i32 s56, s42, 1
	s_sub_i32 s43, s5, s24
	s_cmp_ge_u32 s5, s24
	s_cselect_b32 s42, s56, s42
	s_cselect_b32 s5, s43, s5
	s_add_i32 s43, s42, 1
	s_cmp_ge_u32 s5, s24
	s_cselect_b32 s5, s43, s42
	s_xor_b32 s5, s5, s41
	s_sub_i32 s24, s5, s41
	s_mul_i32 s5, s24, s40
	s_sub_i32 s4, s4, s5
	s_add_i32 s40, s4, s25

.LBB0_481:
	s_add_u32 s50, s0, 0xfff80080
	s_addc_u32 s51, s1, -1
	s_add_i32 s56, 0, 0x10000
	v_add_u32_e32 v142, s56, v170
	ds_read_b128 v[130:133], v142
	ds_read_b128 v[134:137], v142 offset:1024
	ds_read_b128 v[138:141], v142 offset:2048
	ds_read_b128 v[142:145], v142 offset:3072
	s_cmp_eq_u32 s65, 28
	s_cselect_b32 s77, s4, s51
	s_cselect_b32 s76, s5, s50
	s_cselect_b32 s51, s25, s64
	s_cselect_b32 s50, s41, s63
	v_lshl_add_u64 v[168:169], s[0:1], 0, v[164:165]
	s_add_i32 m0, s35, 0xc000
	ds_read_b128 v[174:177], v172
	ds_read_b128 v[178:181], v172 offset:1024
	ds_read_b128 v[182:185], v172 offset:2048
	ds_read_b128 v[186:189], v172 offset:3072
	ds_read_b128 v[190:193], v172 offset:4096
	ds_read_b128 v[194:197], v172 offset:5120
	ds_read_b128 v[198:201], v172 offset:6144
	ds_read_b128 v[202:205], v172 offset:7168
	global_load_lds_dwordx4 v[168:169], off
	v_lshl_add_u64 v[168:169], s[0:1], 0, v[166:167]
	s_add_i32 m0, s35, 0xe000
	s_nop 0
	global_load_lds_dwordx4 v[168:169], off
	s_waitcnt lgkmcnt(8)
	s_barrier
	s_waitcnt lgkmcnt(0)
	s_waitcnt lgkmcnt(0)
	v_mfma_f32_16x16x32_bf16 v[126:129], v[130:133], v[174:177], v[126:129]
	v_mfma_f32_16x16x32_bf16 v[122:125], v[138:141], v[174:177], v[122:125]
	v_mfma_f32_16x16x32_bf16 v[114:117], v[130:133], v[182:185], v[114:117]
	v_mfma_f32_16x16x32_bf16 v[110:113], v[138:141], v[182:185], v[110:113]
	v_mfma_f32_16x16x32_bf16 v[98:101], v[130:133], v[190:193], v[98:101]
	v_mfma_f32_16x16x32_bf16 v[94:97], v[138:141], v[190:193], v[94:97]
	v_mfma_f32_16x16x32_bf16 v[82:85], v[130:133], v[198:201], v[82:85]
	v_mfma_f32_16x16x32_bf16 v[78:81], v[138:141], v[198:201], v[78:81]
	v_mfma_f32_16x16x32_bf16 v[126:129], v[134:137], v[178:181], v[126:129]
	v_mfma_f32_16x16x32_bf16 v[122:125], v[142:145], v[178:181], v[122:125]
	v_mfma_f32_16x16x32_bf16 v[114:117], v[134:137], v[186:189], v[114:117]
	v_mfma_f32_16x16x32_bf16 v[110:113], v[142:145], v[186:189], v[110:113]
	v_mfma_f32_16x16x32_bf16 v[98:101], v[134:137], v[194:197], v[98:101]
	v_mfma_f32_16x16x32_bf16 v[94:97], v[142:145], v[194:197], v[94:97]
	v_mfma_f32_16x16x32_bf16 v[82:85], v[134:137], v[202:205], v[82:85]
	v_mfma_f32_16x16x32_bf16 v[78:81], v[142:145], v[202:205], v[78:81]
	s_barrier
	s_add_i32 s57, 0, 0x14000
	v_add_u32_e32 v168, s57, v170
	s_add_i32 s56, s56, s46
	ds_read_b128 v[234:237], v168
	ds_read_b128 v[238:241], v168 offset:1024
	ds_read_b128 v[242:245], v168 offset:2048
	ds_read_b128 v[246:249], v168 offset:3072
	v_lshl_add_u64 v[168:169], s[50:51], 0, v[210:211]
	s_mov_b32 m0, s56
	v_lshl_add_u64 v[218:219], s[50:51], 0, v[146:147]
	global_load_lds_dwordx4 v[168:169], off
	s_add_i32 m0, s56, 0x2000
	s_nop 0
	global_load_lds_dwordx4 v[218:219], off
	s_barrier
	s_waitcnt lgkmcnt(0)
	s_waitcnt lgkmcnt(0)
	v_mfma_f32_16x16x32_bf16 v[118:121], v[234:237], v[174:177], v[118:121]
	v_mfma_f32_16x16x32_bf16 v[106:109], v[242:245], v[174:177], v[106:109]
	v_mfma_f32_16x16x32_bf16 v[102:105], v[234:237], v[182:185], v[102:105]
	v_mfma_f32_16x16x32_bf16 v[90:93], v[242:245], v[182:185], v[90:93]
	v_mfma_f32_16x16x32_bf16 v[86:89], v[234:237], v[190:193], v[86:89]
	v_mfma_f32_16x16x32_bf16 v[74:77], v[242:245], v[190:193], v[74:77]
	v_mfma_f32_16x16x32_bf16 v[70:73], v[234:237], v[198:201], v[70:73]
	v_mfma_f32_16x16x32_bf16 v[66:69], v[242:245], v[198:201], v[66:69]
	v_mfma_f32_16x16x32_bf16 v[118:121], v[238:241], v[178:181], v[118:121]
	v_mfma_f32_16x16x32_bf16 v[106:109], v[246:249], v[178:181], v[106:109]
	v_mfma_f32_16x16x32_bf16 v[102:105], v[238:241], v[186:189], v[102:105]
	v_mfma_f32_16x16x32_bf16 v[90:93], v[246:249], v[186:189], v[90:93]
	v_mfma_f32_16x16x32_bf16 v[86:89], v[238:241], v[194:197], v[86:89]
	v_mfma_f32_16x16x32_bf16 v[74:77], v[246:249], v[194:197], v[74:77]
	v_mfma_f32_16x16x32_bf16 v[70:73], v[238:241], v[202:205], v[70:73]
	v_mfma_f32_16x16x32_bf16 v[66:69], v[246:249], v[202:205], v[66:69]
	s_mov_b32 m0, s35
	v_lshl_add_u64 v[250:251], s[76:77], 0, v[210:211]
	s_barrier
	ds_read_b128 v[174:177], v172 offset:16384
	ds_read_b128 v[178:181], v172 offset:17408
	ds_read_b128 v[182:185], v172 offset:18432
	ds_read_b128 v[186:189], v172 offset:19456
	ds_read_b128 v[190:193], v172 offset:20480
	ds_read_b128 v[194:197], v172 offset:21504
	ds_read_b128 v[198:201], v172 offset:22528
	ds_read_b128 v[202:205], v172 offset:23552
	global_load_lds_dwordx4 v[250:251], off
	v_lshl_add_u64 v[226:227], s[76:77], 0, v[146:147]
	s_mov_b32 m0, s75
	s_nop 0
	global_load_lds_dwordx4 v[226:227], off
	s_barrier
	s_waitcnt lgkmcnt(0)
	s_waitcnt lgkmcnt(0)
	v_mfma_f32_16x16x32_bf16 v[62:65], v[130:133], v[174:177], v[62:65]
	v_mfma_f32_16x16x32_bf16 v[58:61], v[138:141], v[174:177], v[58:61]
	v_mfma_f32_16x16x32_bf16 v[50:53], v[130:133], v[182:185], v[50:53]
	v_mfma_f32_16x16x32_bf16 v[46:49], v[138:141], v[182:185], v[46:49]
	v_mfma_f32_16x16x32_bf16 v[34:37], v[130:133], v[190:193], v[34:37]
	v_mfma_f32_16x16x32_bf16 v[30:33], v[138:141], v[190:193], v[30:33]
	v_mfma_f32_16x16x32_bf16 v[18:21], v[130:133], v[198:201], v[18:21]
	v_mfma_f32_16x16x32_bf16 v[14:17], v[138:141], v[198:201], v[14:17]
	v_mfma_f32_16x16x32_bf16 v[62:65], v[134:137], v[178:181], v[62:65]
	v_mfma_f32_16x16x32_bf16 v[58:61], v[142:145], v[178:181], v[58:61]
	v_mfma_f32_16x16x32_bf16 v[50:53], v[134:137], v[186:189], v[50:53]
	v_mfma_f32_16x16x32_bf16 v[46:49], v[142:145], v[186:189], v[46:49]
	v_mfma_f32_16x16x32_bf16 v[34:37], v[134:137], v[194:197], v[34:37]
	v_mfma_f32_16x16x32_bf16 v[30:33], v[142:145], v[194:197], v[30:33]
	v_mfma_f32_16x16x32_bf16 v[18:21], v[134:137], v[202:205], v[18:21]
	v_mfma_f32_16x16x32_bf16 v[14:17], v[142:145], v[202:205], v[14:17]
	s_barrier
	s_add_u32 s66, s50, 0x80000
	s_addc_u32 s67, s51, 0
	s_add_i32 s56, s57, s46
	v_lshl_add_u64 v[130:131], s[66:67], 0, v[210:211]
	s_mov_b32 m0, s56
	s_nop 0
	global_load_lds_dwordx4 v[130:131], off
	v_lshl_add_u64 v[130:131], s[66:67], 0, v[146:147]
	s_add_i32 m0, s56, 0x2000
	s_nop 0
	global_load_lds_dwordx4 v[130:131], off
	s_waitcnt vmcnt(6)
	s_barrier
	v_mfma_f32_16x16x32_bf16 v[54:57], v[234:237], v[174:177], v[54:57]
	v_mfma_f32_16x16x32_bf16 v[42:45], v[242:245], v[174:177], v[42:45]
	v_mfma_f32_16x16x32_bf16 v[38:41], v[234:237], v[182:185], v[38:41]
	v_mfma_f32_16x16x32_bf16 v[26:29], v[242:245], v[182:185], v[26:29]
	v_mfma_f32_16x16x32_bf16 v[22:25], v[234:237], v[190:193], v[22:25]
	v_mfma_f32_16x16x32_bf16 v[10:13], v[242:245], v[190:193], v[10:13]
	v_mfma_f32_16x16x32_bf16 v[6:9], v[234:237], v[198:201], v[6:9]
	v_mfma_f32_16x16x32_bf16 v[2:5], v[242:245], v[198:201], v[2:5]
	v_mfma_f32_16x16x32_bf16 v[54:57], v[238:241], v[178:181], v[54:57]
	v_mfma_f32_16x16x32_bf16 v[42:45], v[246:249], v[178:181], v[42:45]
	v_mfma_f32_16x16x32_bf16 v[38:41], v[238:241], v[186:189], v[38:41]
	v_mfma_f32_16x16x32_bf16 v[26:29], v[246:249], v[186:189], v[26:29]
	v_mfma_f32_16x16x32_bf16 v[22:25], v[238:241], v[194:197], v[22:25]
	v_mfma_f32_16x16x32_bf16 v[10:13], v[246:249], v[194:197], v[10:13]
	v_mfma_f32_16x16x32_bf16 v[6:9], v[238:241], v[202:205], v[6:9]
	v_mfma_f32_16x16x32_bf16 v[2:5], v[246:249], v[202:205], v[2:5]
	s_add_i32 s56, 0, 0x18000
	v_add_u32_e32 v142, s56, v170
	s_barrier
	ds_read_b128 v[130:133], v142
	ds_read_b128 v[134:137], v142 offset:1024
	ds_read_b128 v[138:141], v142 offset:2048
	ds_read_b128 v[142:145], v142 offset:3072
	s_add_u32 s66, s76, 0x80000
	s_addc_u32 s67, s77, 0
	s_mov_b32 m0, s78
	v_lshl_add_u64 v[234:235], s[66:67], 0, v[210:211]
	ds_read_b128 v[174:177], v172 offset:32768
	ds_read_b128 v[178:181], v172 offset:33792
	ds_read_b128 v[182:185], v172 offset:34816
	ds_read_b128 v[186:189], v172 offset:35840
	ds_read_b128 v[190:193], v172 offset:36864
	ds_read_b128 v[194:197], v172 offset:37888
	ds_read_b128 v[198:201], v172 offset:38912
	ds_read_b128 v[202:205], v172 offset:39936
	global_load_lds_dwordx4 v[234:235], off
	v_lshl_add_u64 v[234:235], s[66:67], 0, v[146:147]
	s_mov_b32 m0, s2
	s_nop 0
	global_load_lds_dwordx4 v[234:235], off
	s_waitcnt lgkmcnt(8)
	s_barrier
	s_waitcnt lgkmcnt(0)
	s_waitcnt lgkmcnt(0)
	v_mfma_f32_16x16x32_bf16 v[126:129], v[130:133], v[174:177], v[126:129]
	v_mfma_f32_16x16x32_bf16 v[122:125], v[138:141], v[174:177], v[122:125]
	v_mfma_f32_16x16x32_bf16 v[114:117], v[130:133], v[182:185], v[114:117]
	v_mfma_f32_16x16x32_bf16 v[110:113], v[138:141], v[182:185], v[110:113]
	v_mfma_f32_16x16x32_bf16 v[98:101], v[130:133], v[190:193], v[98:101]
	v_mfma_f32_16x16x32_bf16 v[94:97], v[138:141], v[190:193], v[94:97]
	v_mfma_f32_16x16x32_bf16 v[82:85], v[130:133], v[198:201], v[82:85]
	v_mfma_f32_16x16x32_bf16 v[78:81], v[138:141], v[198:201], v[78:81]
	v_mfma_f32_16x16x32_bf16 v[126:129], v[134:137], v[178:181], v[126:129]
	v_mfma_f32_16x16x32_bf16 v[122:125], v[142:145], v[178:181], v[122:125]
	v_mfma_f32_16x16x32_bf16 v[114:117], v[134:137], v[186:189], v[114:117]
	v_mfma_f32_16x16x32_bf16 v[110:113], v[142:145], v[186:189], v[110:113]
	v_mfma_f32_16x16x32_bf16 v[98:101], v[134:137], v[194:197], v[98:101]
	v_mfma_f32_16x16x32_bf16 v[94:97], v[142:145], v[194:197], v[94:97]
	v_mfma_f32_16x16x32_bf16 v[82:85], v[134:137], v[202:205], v[82:85]
	v_mfma_f32_16x16x32_bf16 v[78:81], v[142:145], v[202:205], v[78:81]
	s_barrier
	s_add_i32 s57, 0, 0x1c000
	s_add_i32 s56, s56, s46
	v_add_u32_e32 v173, s57, v170
	v_lshl_add_u64 v[168:169], v[168:169], 0, s[36:37]
	s_mov_b32 m0, s56
	ds_read_b128 v[234:237], v173
	ds_read_b128 v[238:241], v173 offset:1024
	ds_read_b128 v[242:245], v173 offset:2048
	ds_read_b128 v[246:249], v173 offset:3072
	global_load_lds_dwordx4 v[168:169], off
	v_lshl_add_u64 v[168:169], v[218:219], 0, s[36:37]
	s_add_i32 m0, s56, 0x2000
	s_nop 0
	global_load_lds_dwordx4 v[168:169], off
	s_barrier
	s_waitcnt lgkmcnt(0)
	s_waitcnt lgkmcnt(0)
	v_mfma_f32_16x16x32_bf16 v[118:121], v[234:237], v[174:177], v[118:121]
	v_mfma_f32_16x16x32_bf16 v[106:109], v[242:245], v[174:177], v[106:109]
	v_mfma_f32_16x16x32_bf16 v[102:105], v[234:237], v[182:185], v[102:105]
	v_mfma_f32_16x16x32_bf16 v[90:93], v[242:245], v[182:185], v[90:93]
	v_mfma_f32_16x16x32_bf16 v[86:89], v[234:237], v[190:193], v[86:89]
	v_mfma_f32_16x16x32_bf16 v[74:77], v[242:245], v[190:193], v[74:77]
	v_mfma_f32_16x16x32_bf16 v[70:73], v[234:237], v[198:201], v[70:73]
	v_mfma_f32_16x16x32_bf16 v[66:69], v[242:245], v[198:201], v[66:69]
	v_mfma_f32_16x16x32_bf16 v[118:121], v[238:241], v[178:181], v[118:121]
	v_mfma_f32_16x16x32_bf16 v[106:109], v[246:249], v[178:181], v[106:109]
	v_mfma_f32_16x16x32_bf16 v[102:105], v[238:241], v[186:189], v[102:105]
	v_mfma_f32_16x16x32_bf16 v[90:93], v[246:249], v[186:189], v[90:93]
	v_mfma_f32_16x16x32_bf16 v[86:89], v[238:241], v[194:197], v[86:89]
	v_mfma_f32_16x16x32_bf16 v[74:77], v[246:249], v[194:197], v[74:77]
	v_mfma_f32_16x16x32_bf16 v[70:73], v[238:241], v[202:205], v[70:73]
	v_mfma_f32_16x16x32_bf16 v[66:69], v[246:249], v[202:205], v[66:69]
	s_mov_b32 m0, s27
	v_lshl_add_u64 v[168:169], v[250:251], 0, s[36:37]
	s_barrier
	ds_read_b128 v[174:177], v172 offset:49152
	ds_read_b128 v[178:181], v172 offset:50176
	ds_read_b128 v[182:185], v172 offset:51200
	ds_read_b128 v[186:189], v172 offset:52224
	ds_read_b128 v[190:193], v172 offset:53248
	ds_read_b128 v[194:197], v172 offset:54272
	ds_read_b128 v[198:201], v172 offset:55296
	ds_read_b128 v[202:205], v172 offset:56320
	global_load_lds_dwordx4 v[168:169], off
	v_lshl_add_u64 v[168:169], v[226:227], 0, s[36:37]
	s_mov_b32 m0, s28
	s_nop 0
	global_load_lds_dwordx4 v[168:169], off
	s_barrier
	s_waitcnt lgkmcnt(0)
	s_waitcnt lgkmcnt(0)
	v_mfma_f32_16x16x32_bf16 v[62:65], v[130:133], v[174:177], v[62:65]
	v_mfma_f32_16x16x32_bf16 v[58:61], v[138:141], v[174:177], v[58:61]
	v_mfma_f32_16x16x32_bf16 v[50:53], v[130:133], v[182:185], v[50:53]
	v_mfma_f32_16x16x32_bf16 v[46:49], v[138:141], v[182:185], v[46:49]
	v_mfma_f32_16x16x32_bf16 v[34:37], v[130:133], v[190:193], v[34:37]
	v_mfma_f32_16x16x32_bf16 v[30:33], v[138:141], v[190:193], v[30:33]
	v_mfma_f32_16x16x32_bf16 v[18:21], v[130:133], v[198:201], v[18:21]
	v_mfma_f32_16x16x32_bf16 v[14:17], v[138:141], v[198:201], v[14:17]
	v_mfma_f32_16x16x32_bf16 v[62:65], v[134:137], v[178:181], v[62:65]
	v_mfma_f32_16x16x32_bf16 v[58:61], v[142:145], v[178:181], v[58:61]
	v_mfma_f32_16x16x32_bf16 v[50:53], v[134:137], v[186:189], v[50:53]
	v_mfma_f32_16x16x32_bf16 v[46:49], v[142:145], v[186:189], v[46:49]
	v_mfma_f32_16x16x32_bf16 v[34:37], v[134:137], v[194:197], v[34:37]
	v_mfma_f32_16x16x32_bf16 v[30:33], v[142:145], v[194:197], v[30:33]
	v_mfma_f32_16x16x32_bf16 v[18:21], v[134:137], v[202:205], v[18:21]
	v_mfma_f32_16x16x32_bf16 v[14:17], v[142:145], v[202:205], v[14:17]
	s_barrier
	s_add_u32 s50, s50, 0x80080
	s_addc_u32 s51, s51, 0
	s_add_i32 s56, s57, s46
	v_lshl_add_u64 v[130:131], s[50:51], 0, v[210:211]
	s_mov_b32 m0, s56
	s_nop 0
	global_load_lds_dwordx4 v[130:131], off
	v_lshl_add_u64 v[130:131], s[50:51], 0, v[146:147]
	s_add_i32 m0, s56, 0x2000
	s_nop 0
	global_load_lds_dwordx4 v[130:131], off
	s_waitcnt vmcnt(6)
	s_barrier
	v_mfma_f32_16x16x32_bf16 v[54:57], v[234:237], v[174:177], v[54:57]
	v_mfma_f32_16x16x32_bf16 v[42:45], v[242:245], v[174:177], v[42:45]
	v_mfma_f32_16x16x32_bf16 v[38:41], v[234:237], v[182:185], v[38:41]
	v_mfma_f32_16x16x32_bf16 v[26:29], v[242:245], v[182:185], v[26:29]
	v_mfma_f32_16x16x32_bf16 v[22:25], v[234:237], v[190:193], v[22:25]
	v_mfma_f32_16x16x32_bf16 v[10:13], v[242:245], v[190:193], v[10:13]
	v_mfma_f32_16x16x32_bf16 v[6:9], v[234:237], v[198:201], v[6:9]
	v_mfma_f32_16x16x32_bf16 v[2:5], v[242:245], v[198:201], v[2:5]
	v_mfma_f32_16x16x32_bf16 v[54:57], v[238:241], v[178:181], v[54:57]
	v_mfma_f32_16x16x32_bf16 v[42:45], v[246:249], v[178:181], v[42:45]
	v_mfma_f32_16x16x32_bf16 v[38:41], v[238:241], v[186:189], v[38:41]
	v_mfma_f32_16x16x32_bf16 v[26:29], v[246:249], v[186:189], v[26:29]
	v_mfma_f32_16x16x32_bf16 v[22:25], v[238:241], v[194:197], v[22:25]
	v_mfma_f32_16x16x32_bf16 v[10:13], v[246:249], v[194:197], v[10:13]
	v_mfma_f32_16x16x32_bf16 v[6:9], v[238:241], v[202:205], v[6:9]
	v_mfma_f32_16x16x32_bf16 v[2:5], v[246:249], v[202:205], v[2:5]
	s_add_i32 s65, s65, 2
	s_add_u32 s0, s0, 0x100
	s_addc_u32 s1, s1, 0
	s_add_u32 s63, s63, 0x100
	s_addc_u32 s64, s64, 0
	s_cmp_gt_u32 s65, 29
	s_barrier
	s_cbranch_scc0 .LBB0_481
	s_mul_hi_i32 s0, s74, 0x7e07e07f
	s_lshr_b32 s1, s0, 31
	s_ashr_i32 s4, s0, 5
	s_add_i32 s4, s4, s1
	s_mul_i32 s0, s4, 0xffffffbf
	s_add_i32 s0, s0, s74
	s_cmp_lg_u32 s0, 0
	s_cbranch_scc0 .LBB0_484
	s_lshl_b32 s1, s4, 14
	s_lshl_b32 s0, s0, 8
	s_add_i32 s0, s1, s0
	s_addk_i32 s0, 0xff00
	s_ashr_i32 s1, s0, 31
	s_lshl_b64 s[50:51], s[0:1], 13
	s_add_u32 s0, s6, s50
	s_addc_u32 s1, s3, s51
	s_add_u32 s50, s18, s50
	s_mul_i32 s62, s4, 0x3000
	s_addc_u32 s51, s19, s51
	s_ashr_i32 s63, s62, 31
	s_lshl_b64 s[62:63], s[62:63], 2
	s_add_u32 s5, s61, s62
	s_addc_u32 s25, s26, s63
	s_add_u32 s62, s5, 0x4000
	s_addc_u32 s63, s25, 0
	s_cbranch_execnz .LBB0_477
	s_branch .LBB0_485

.LBB0_489:
	s_setprio 0
	s_waitcnt vmcnt(0)
	s_waitcnt lgkmcnt(0)
	s_barrier
	s_and_saveexec_b64 s[0:1], s[44:45]
	s_cbranch_execz .LBB0_537
	v_readlane_b32 s2, v255, 29
	s_waitcnt vmcnt(0) expcnt(0) lgkmcnt(0)
	s_nop 0
	v_mov_b32_e32 v2, s2
	ds_read_b32 v4, v2
	v_readlane_b32 s2, v255, 30
	s_waitcnt lgkmcnt(0)
	v_cmp_ne_u32_e32 vcc, 0, v4
	v_mov_b32_e32 v2, s2
	ds_read_b32 v2, v2
	s_cbranch_vccnz .LBB0_505
	v_readlane_b32 s4, v253, 16
	v_readlane_b32 s5, v253, 17
	s_load_dwordx2 s[2:3], s[4:5], 0x4
	s_waitcnt lgkmcnt(0)
	s_mul_i32 s2, s2, s86
	s_mul_i32 s2, s2, s3
	s_mov_b32 s3, 1
	s_branch .LBB0_493

.LBB0_608:
	v_lshrrev_b32_e32 v18, 1, v8
	v_and_b32_e32 v18, 24, v18
	s_lshl_b32 s0, s0, 5
	v_and_b32_e32 v9, 15, v8
	v_lshlrev_b32_e32 v19, 1, v18
	v_lshlrev_b32_e32 v8, 2, v8
	s_and_b32 s4, s0, 0x60
	v_lshl_add_u64 v[10:11], s[50:51], 0, v[210:211]
	v_mov_b32_e32 v131, v211
	v_lshl_or_b32 v142, s1, 6, v9
	v_lshl_or_b32 v9, v9, 6, v19
	s_lshl_b32 s1, s1, 13
	v_and_b32_e32 v8, 32, v8
	s_lshl_b32 s0, s4, 7
	v_lshl_add_u64 v[12:13], s[50:51], 0, v[130:131]
	v_mov_b32_e32 v135, v211
	v_bitop3_b32 v19, v9, s1, v8 bitop3:0xde
	v_bitop3_b32 v143, v9, s0, v8 bitop3:0xde
	s_add_i32 m0, s6, 0x18000
	v_lshl_add_u64 v[8:9], v[10:11], 0, s[36:37]
	v_lshl_add_u64 v[14:15], s[62:63], 0, v[134:135]
	v_mov_b32_e32 v133, v211
	s_waitcnt vmcnt(4)
	s_barrier
	global_load_lds_dwordx4 v[8:9], off
	v_lshl_add_u64 v[8:9], v[12:13], 0, s[36:37]
	s_add_i32 m0, s6, 0x1a000
	s_add_i32 s28, s6, 0x8000
	s_add_i32 s29, s6, 0xa000
	v_lshl_add_u64 v[16:17], s[62:63], 0, v[132:133]
	global_load_lds_dwordx4 v[8:9], off
	v_lshl_add_u64 v[8:9], v[14:15], 0, s[36:37]
	s_mov_b32 m0, s28
	s_add_u32 s0, s50, 0x80080
	global_load_lds_dwordx4 v[8:9], off
	v_lshl_add_u64 v[8:9], v[16:17], 0, s[36:37]
	s_mov_b32 m0, s29
	s_addc_u32 s1, s51, 0
	global_load_lds_dwordx4 v[8:9], off
	s_add_i32 m0, s6, 0x1c000
	v_lshl_add_u64 v[8:9], s[0:1], 0, v[210:211]
	global_load_lds_dwordx4 v[8:9], off
	v_lshl_add_u64 v[8:9], s[0:1], 0, v[130:131]
	s_add_i32 m0, s6, 0x1e000
	v_or_b32_e32 v144, s4, v18
	global_load_lds_dwordx4 v[8:9], off
	v_lshlrev_b32_e32 v8, 15, v6
	v_and_b32_e32 v8, 0xffff0000, v8
	v_lshl_add_u32 v5, v5, 12, v8
	v_and_b32_e32 v6, 1, v6
	v_lshl_or_b32 v5, v6, 6, v5
	v_lshl_add_u32 v136, v7, 1, v5
	v_lshlrev_b32_e32 v5, 15, v2
	v_and_b32_e32 v5, 0xffff0000, v5
	s_waitcnt vmcnt(6)
	v_lshl_add_u32 v3, v3, 12, v5
	v_and_b32_e32 v2, 1, v2
	v_lshl_or_b32 v2, v2, 6, v3
	v_mov_b32_e32 v137, v211
	v_lshl_add_u32 v138, v4, 1, v2
	v_mov_b32_e32 v139, v211
	s_mov_b32 s43, 0
	v_add_u32_e32 v145, 0, v19
	s_barrier
.LBB0_609:
	v_readfirstlane_b32 s98, v0
	s_nop 3
	s_cmp_ge_u32 s98, 0x100
	s_cbranch_scc0 .Lgp_g8
	s_setprio 1
.Lgp_g8:
	s_add_i32 s43, s43, 1
	s_mul_i32 s0, s43, s87
	s_mul_hi_u32 s1, s43, s86
	s_add_i32 s1, s1, s0
	s_mul_i32 s0, s43, s86
	s_add_u32 s34, s0, s70
	s_addc_u32 s35, s1, s71
	v_mov_b64_e32 v[2:3], s[80:81]
	v_cmp_ge_i64_e64 s[38:39], s[34:35], v[2:3]
	v_cmp_lt_i64_e64 s[0:1], s[34:35], v[2:3]
	s_and_b64 vcc, exec, s[38:39]
	s_cbranch_vccnz .LBB0_611
	s_ashr_i32 s4, s34, 31
	s_lshr_b32 s4, s4, 29
	s_add_i32 s4, s34, s4
	s_ashr_i32 s5, s4, 3
	s_and_b32 s4, s4, -8
	s_sub_i32 s4, s34, s4
	s_cmp_lt_i32 s4, 0
	s_cselect_b32 s10, s3, s2
	s_mul_i32 s4, s10, s4
	s_add_i32 s4, s4, s5
	s_ashr_i32 s5, s4, 31
	s_lshr_b32 s5, s5, 27
	s_add_i32 s5, s4, s5
	s_ashr_i32 s10, s5, 5
	s_lshl_b32 s11, s10, 3
	s_sub_i32 s10, s84, s11
	s_min_i32 s24, s10, 8
	s_abs_i32 s10, s24
	v_cvt_f32_u32_e32 v2, s10
	s_sub_i32 s34, 0, s10
	s_andn2_b32 s5, s5, 31
	s_sub_i32 s4, s4, s5
	v_rcp_iflag_f32_e32 v2, v2
	s_abs_i32 s5, s4
	s_xor_b32 s25, s4, s24
	s_ashr_i32 s25, s25, 31
	v_mul_f32_e32 v2, 0x4f7ffffe, v2
	v_cvt_u32_f32_e32 v2, v2
	s_nop 0
	v_readfirstlane_b32 s35, v2
	s_mul_i32 s34, s34, s35
	s_mul_hi_u32 s34, s35, s34
	s_add_i32 s35, s35, s34
	s_mul_hi_u32 s34, s5, s35
	s_mul_i32 s35, s34, s10
	s_sub_i32 s5, s5, s35
	s_add_i32 s40, s34, 1
	s_sub_i32 s35, s5, s10
	s_cmp_ge_u32 s5, s10
	s_cselect_b32 s34, s40, s34
	s_cselect_b32 s5, s35, s5
	s_add_i32 s35, s34, 1
	s_cmp_ge_u32 s5, s10
	s_cselect_b32 s5, s35, s34
	s_xor_b32 s5, s5, s25
	s_sub_i32 s10, s5, s25
	s_mul_i32 s5, s10, s24
	s_sub_i32 s4, s4, s5
	s_add_i32 s24, s4, s11

.LBB0_612:
	s_add_u32 s50, s0, 0xfff80080
	s_addc_u32 s51, s1, -1
	s_add_i32 s56, 0, 0x10000
	v_add_u32_e32 v140, s56, v143
	ds_read_b128 v[146:149], v140
	ds_read_b128 v[150:153], v140 offset:1024
	ds_read_b128 v[154:157], v140 offset:2048
	ds_read_b128 v[158:161], v140 offset:3072
	s_cmp_eq_u32 s61, 28
	s_cselect_b32 s63, s4, s51
	s_cselect_b32 s62, s5, s50
	s_cselect_b32 s51, s11, s53
	s_cselect_b32 s50, s25, s52
	v_lshl_add_u64 v[140:141], s[0:1], 0, v[136:137]
	s_add_i32 m0, s6, 0xc000
	ds_read_b128 v[162:165], v145
	ds_read_b128 v[166:169], v145 offset:1024
	ds_read_b128 v[170:173], v145 offset:2048
	ds_read_b128 v[174:177], v145 offset:3072
	ds_read_b128 v[178:181], v145 offset:4096
	ds_read_b128 v[182:185], v145 offset:5120
	ds_read_b128 v[186:189], v145 offset:6144
	ds_read_b128 v[190:193], v145 offset:7168
	global_load_lds_dwordx4 v[140:141], off
	v_lshl_add_u64 v[140:141], s[0:1], 0, v[138:139]
	s_add_i32 m0, s6, 0xe000
	s_nop 0
	global_load_lds_dwordx4 v[140:141], off
	s_waitcnt lgkmcnt(8)
	s_barrier
	s_waitcnt lgkmcnt(0)
	s_waitcnt lgkmcnt(0)
	v_mfma_f32_16x16x32_bf16 v[126:129], v[146:149], v[162:165], v[126:129]
	v_mfma_f32_16x16x32_bf16 v[122:125], v[154:157], v[162:165], v[122:125]
	v_mfma_f32_16x16x32_bf16 v[114:117], v[146:149], v[170:173], v[114:117]
	v_mfma_f32_16x16x32_bf16 v[106:109], v[154:157], v[170:173], v[106:109]
	v_mfma_f32_16x16x32_bf16 v[98:101], v[146:149], v[178:181], v[98:101]
	v_mfma_f32_16x16x32_bf16 v[90:93], v[154:157], v[178:181], v[90:93]
	v_mfma_f32_16x16x32_bf16 v[82:85], v[146:149], v[186:189], v[82:85]
	v_mfma_f32_16x16x32_bf16 v[74:77], v[154:157], v[186:189], v[74:77]
	v_mfma_f32_16x16x32_bf16 v[126:129], v[150:153], v[166:169], v[126:129]
	v_mfma_f32_16x16x32_bf16 v[122:125], v[158:161], v[166:169], v[122:125]
	v_mfma_f32_16x16x32_bf16 v[114:117], v[150:153], v[174:177], v[114:117]
	v_mfma_f32_16x16x32_bf16 v[106:109], v[158:161], v[174:177], v[106:109]
	v_mfma_f32_16x16x32_bf16 v[98:101], v[150:153], v[182:185], v[98:101]
	v_mfma_f32_16x16x32_bf16 v[90:93], v[158:161], v[182:185], v[90:93]
	v_mfma_f32_16x16x32_bf16 v[82:85], v[150:153], v[190:193], v[82:85]
	v_mfma_f32_16x16x32_bf16 v[74:77], v[158:161], v[190:193], v[74:77]
	s_barrier
	s_add_i32 s57, 0, 0x14000
	v_add_u32_e32 v140, s57, v143
	s_add_i32 s56, s56, s76
	ds_read_b128 v[194:197], v140
	ds_read_b128 v[198:201], v140 offset:1024
	ds_read_b128 v[202:205], v140 offset:2048
	ds_read_b128 v[234:237], v140 offset:3072
	v_lshl_add_u64 v[140:141], s[50:51], 0, v[210:211]
	s_mov_b32 m0, s56
	v_lshl_add_u64 v[218:219], s[50:51], 0, v[130:131]
	global_load_lds_dwordx4 v[140:141], off
	s_add_i32 m0, s56, 0x2000
	s_nop 0
	global_load_lds_dwordx4 v[218:219], off
	s_barrier
	s_waitcnt lgkmcnt(0)
	s_waitcnt lgkmcnt(0)
	v_mfma_f32_16x16x32_bf16 v[118:121], v[194:197], v[162:165], v[118:121]
	v_mfma_f32_16x16x32_bf16 v[110:113], v[202:205], v[162:165], v[110:113]
	v_mfma_f32_16x16x32_bf16 v[102:105], v[194:197], v[170:173], v[102:105]
	v_mfma_f32_16x16x32_bf16 v[94:97], v[202:205], v[170:173], v[94:97]
	v_mfma_f32_16x16x32_bf16 v[86:89], v[194:197], v[178:181], v[86:89]
	v_mfma_f32_16x16x32_bf16 v[78:81], v[202:205], v[178:181], v[78:81]
	v_mfma_f32_16x16x32_bf16 v[70:73], v[194:197], v[186:189], v[70:73]
	v_mfma_f32_16x16x32_bf16 v[66:69], v[202:205], v[186:189], v[66:69]
	v_mfma_f32_16x16x32_bf16 v[118:121], v[198:201], v[166:169], v[118:121]
	v_mfma_f32_16x16x32_bf16 v[110:113], v[234:237], v[166:169], v[110:113]
	v_mfma_f32_16x16x32_bf16 v[102:105], v[198:201], v[174:177], v[102:105]
	v_mfma_f32_16x16x32_bf16 v[94:97], v[234:237], v[174:177], v[94:97]
	v_mfma_f32_16x16x32_bf16 v[86:89], v[198:201], v[182:185], v[86:89]
	v_mfma_f32_16x16x32_bf16 v[78:81], v[234:237], v[182:185], v[78:81]
	v_mfma_f32_16x16x32_bf16 v[70:73], v[198:201], v[190:193], v[70:73]
	v_mfma_f32_16x16x32_bf16 v[66:69], v[234:237], v[190:193], v[66:69]
	s_mov_b32 m0, s6
	v_lshl_add_u64 v[226:227], s[62:63], 0, v[134:135]
	s_barrier
	ds_read_b128 v[162:165], v145 offset:16384
	ds_read_b128 v[166:169], v145 offset:17408
	ds_read_b128 v[170:173], v145 offset:18432
	ds_read_b128 v[174:177], v145 offset:19456
	ds_read_b128 v[178:181], v145 offset:20480
	ds_read_b128 v[182:185], v145 offset:21504
	ds_read_b128 v[186:189], v145 offset:22528
	ds_read_b128 v[190:193], v145 offset:23552
	global_load_lds_dwordx4 v[226:227], off
	v_lshl_add_u64 v[238:239], s[62:63], 0, v[132:133]
	s_mov_b32 m0, s7
	s_nop 0
	global_load_lds_dwordx4 v[238:239], off
	s_barrier
	s_waitcnt lgkmcnt(0)
	s_waitcnt lgkmcnt(0)
	v_mfma_f32_16x16x32_bf16 v[62:65], v[146:149], v[162:165], v[62:65]
	v_mfma_f32_16x16x32_bf16 v[58:61], v[154:157], v[162:165], v[58:61]
	v_mfma_f32_16x16x32_bf16 v[50:53], v[146:149], v[170:173], v[50:53]
	v_mfma_f32_16x16x32_bf16 v[42:45], v[154:157], v[170:173], v[42:45]
	v_mfma_f32_16x16x32_bf16 v[34:37], v[146:149], v[178:181], v[34:37]
	v_mfma_f32_16x16x32_bf16 v[26:29], v[154:157], v[178:181], v[26:29]
	v_mfma_f32_16x16x32_bf16 v[18:21], v[146:149], v[186:189], v[18:21]
	v_mfma_f32_16x16x32_bf16 v[10:13], v[154:157], v[186:189], v[10:13]
	v_mfma_f32_16x16x32_bf16 v[62:65], v[150:153], v[166:169], v[62:65]
	v_mfma_f32_16x16x32_bf16 v[58:61], v[158:161], v[166:169], v[58:61]
	v_mfma_f32_16x16x32_bf16 v[50:53], v[150:153], v[174:177], v[50:53]
	v_mfma_f32_16x16x32_bf16 v[42:45], v[158:161], v[174:177], v[42:45]
	v_mfma_f32_16x16x32_bf16 v[34:37], v[150:153], v[182:185], v[34:37]
	v_mfma_f32_16x16x32_bf16 v[26:29], v[158:161], v[182:185], v[26:29]
	v_mfma_f32_16x16x32_bf16 v[18:21], v[150:153], v[190:193], v[18:21]
	v_mfma_f32_16x16x32_bf16 v[10:13], v[158:161], v[190:193], v[10:13]
	s_barrier
	s_add_u32 s64, s50, 0x80000
	s_addc_u32 s65, s51, 0
	s_add_i32 s56, s57, s76
	v_lshl_add_u64 v[146:147], s[64:65], 0, v[210:211]
	s_mov_b32 m0, s56
	s_nop 0
	global_load_lds_dwordx4 v[146:147], off
	v_lshl_add_u64 v[146:147], s[64:65], 0, v[130:131]
	s_add_i32 m0, s56, 0x2000
	s_nop 0
	global_load_lds_dwordx4 v[146:147], off
	s_waitcnt vmcnt(6)
	s_barrier
	v_mfma_f32_16x16x32_bf16 v[54:57], v[194:197], v[162:165], v[54:57]
	v_mfma_f32_16x16x32_bf16 v[46:49], v[202:205], v[162:165], v[46:49]
	v_mfma_f32_16x16x32_bf16 v[38:41], v[194:197], v[170:173], v[38:41]
	v_mfma_f32_16x16x32_bf16 v[30:33], v[202:205], v[170:173], v[30:33]
	v_mfma_f32_16x16x32_bf16 v[22:25], v[194:197], v[178:181], v[22:25]
	v_mfma_f32_16x16x32_bf16 v[14:17], v[202:205], v[178:181], v[14:17]
	v_mfma_f32_16x16x32_bf16 v[6:9], v[194:197], v[186:189], v[6:9]
	v_mfma_f32_16x16x32_bf16 v[2:5], v[202:205], v[186:189], v[2:5]
	v_mfma_f32_16x16x32_bf16 v[54:57], v[198:201], v[166:169], v[54:57]
	v_mfma_f32_16x16x32_bf16 v[46:49], v[234:237], v[166:169], v[46:49]
	v_mfma_f32_16x16x32_bf16 v[38:41], v[198:201], v[174:177], v[38:41]
	v_mfma_f32_16x16x32_bf16 v[30:33], v[234:237], v[174:177], v[30:33]
	v_mfma_f32_16x16x32_bf16 v[22:25], v[198:201], v[182:185], v[22:25]
	v_mfma_f32_16x16x32_bf16 v[14:17], v[234:237], v[182:185], v[14:17]
	v_mfma_f32_16x16x32_bf16 v[6:9], v[198:201], v[190:193], v[6:9]
	v_mfma_f32_16x16x32_bf16 v[2:5], v[234:237], v[190:193], v[2:5]
	s_add_i32 s56, 0, 0x18000
	v_add_u32_e32 v158, s56, v143
	s_barrier
	ds_read_b128 v[146:149], v158
	ds_read_b128 v[150:153], v158 offset:1024
	ds_read_b128 v[154:157], v158 offset:2048
	ds_read_b128 v[158:161], v158 offset:3072
	s_add_u32 s62, s62, 0x80000
	s_addc_u32 s63, s63, 0
	s_mov_b32 m0, s26
	v_lshl_add_u64 v[194:195], s[62:63], 0, v[134:135]
	ds_read_b128 v[162:165], v145 offset:32768
	ds_read_b128 v[166:169], v145 offset:33792
	ds_read_b128 v[170:173], v145 offset:34816
	ds_read_b128 v[174:177], v145 offset:35840
	ds_read_b128 v[178:181], v145 offset:36864
	ds_read_b128 v[182:185], v145 offset:37888
	ds_read_b128 v[186:189], v145 offset:38912
	ds_read_b128 v[190:193], v145 offset:39936
	global_load_lds_dwordx4 v[194:195], off
	v_lshl_add_u64 v[194:195], s[62:63], 0, v[132:133]
	s_mov_b32 m0, s27
	s_nop 0
	global_load_lds_dwordx4 v[194:195], off
	s_waitcnt lgkmcnt(8)
	s_barrier
	s_waitcnt lgkmcnt(0)
	s_waitcnt lgkmcnt(0)
	v_mfma_f32_16x16x32_bf16 v[126:129], v[146:149], v[162:165], v[126:129]
	v_mfma_f32_16x16x32_bf16 v[122:125], v[154:157], v[162:165], v[122:125]
	v_mfma_f32_16x16x32_bf16 v[114:117], v[146:149], v[170:173], v[114:117]
	v_mfma_f32_16x16x32_bf16 v[106:109], v[154:157], v[170:173], v[106:109]
	v_mfma_f32_16x16x32_bf16 v[98:101], v[146:149], v[178:181], v[98:101]
	v_mfma_f32_16x16x32_bf16 v[90:93], v[154:157], v[178:181], v[90:93]
	v_mfma_f32_16x16x32_bf16 v[82:85], v[146:149], v[186:189], v[82:85]
	v_mfma_f32_16x16x32_bf16 v[74:77], v[154:157], v[186:189], v[74:77]
	v_mfma_f32_16x16x32_bf16 v[126:129], v[150:153], v[166:169], v[126:129]
	v_mfma_f32_16x16x32_bf16 v[122:125], v[158:161], v[166:169], v[122:125]
	v_mfma_f32_16x16x32_bf16 v[114:117], v[150:153], v[174:177], v[114:117]
	v_mfma_f32_16x16x32_bf16 v[106:109], v[158:161], v[174:177], v[106:109]
	v_mfma_f32_16x16x32_bf16 v[98:101], v[150:153], v[182:185], v[98:101]
	v_mfma_f32_16x16x32_bf16 v[90:93], v[158:161], v[182:185], v[90:93]
	v_mfma_f32_16x16x32_bf16 v[82:85], v[150:153], v[190:193], v[82:85]
	v_mfma_f32_16x16x32_bf16 v[74:77], v[158:161], v[190:193], v[74:77]
	s_barrier
	s_add_i32 s57, 0, 0x1c000
	s_add_i32 s56, s56, s76
	v_add_u32_e32 v233, s57, v143
	v_lshl_add_u64 v[140:141], v[140:141], 0, s[36:37]
	s_mov_b32 m0, s56
	ds_read_b128 v[194:197], v233
	ds_read_b128 v[198:201], v233 offset:1024
	ds_read_b128 v[202:205], v233 offset:2048
	ds_read_b128 v[234:237], v233 offset:3072
	global_load_lds_dwordx4 v[140:141], off
	v_lshl_add_u64 v[140:141], v[218:219], 0, s[36:37]
	s_add_i32 m0, s56, 0x2000
	s_nop 0
	global_load_lds_dwordx4 v[140:141], off
	s_barrier
	s_waitcnt lgkmcnt(0)
	s_waitcnt lgkmcnt(0)
	v_mfma_f32_16x16x32_bf16 v[118:121], v[194:197], v[162:165], v[118:121]
	v_mfma_f32_16x16x32_bf16 v[110:113], v[202:205], v[162:165], v[110:113]
	v_mfma_f32_16x16x32_bf16 v[102:105], v[194:197], v[170:173], v[102:105]
	v_mfma_f32_16x16x32_bf16 v[94:97], v[202:205], v[170:173], v[94:97]
	v_mfma_f32_16x16x32_bf16 v[86:89], v[194:197], v[178:181], v[86:89]
	v_mfma_f32_16x16x32_bf16 v[78:81], v[202:205], v[178:181], v[78:81]
	v_mfma_f32_16x16x32_bf16 v[70:73], v[194:197], v[186:189], v[70:73]
	v_mfma_f32_16x16x32_bf16 v[66:69], v[202:205], v[186:189], v[66:69]
	v_mfma_f32_16x16x32_bf16 v[118:121], v[198:201], v[166:169], v[118:121]
	v_mfma_f32_16x16x32_bf16 v[110:113], v[234:237], v[166:169], v[110:113]
	v_mfma_f32_16x16x32_bf16 v[102:105], v[198:201], v[174:177], v[102:105]
	v_mfma_f32_16x16x32_bf16 v[94:97], v[234:237], v[174:177], v[94:97]
	v_mfma_f32_16x16x32_bf16 v[86:89], v[198:201], v[182:185], v[86:89]
	v_mfma_f32_16x16x32_bf16 v[78:81], v[234:237], v[182:185], v[78:81]
	v_mfma_f32_16x16x32_bf16 v[70:73], v[198:201], v[190:193], v[70:73]
	v_mfma_f32_16x16x32_bf16 v[66:69], v[234:237], v[190:193], v[66:69]
	s_mov_b32 m0, s28
	v_lshl_add_u64 v[140:141], v[226:227], 0, s[36:37]
	s_barrier
	ds_read_b128 v[162:165], v145 offset:49152
	ds_read_b128 v[166:169], v145 offset:50176
	ds_read_b128 v[170:173], v145 offset:51200
	ds_read_b128 v[174:177], v145 offset:52224
	ds_read_b128 v[178:181], v145 offset:53248
	ds_read_b128 v[182:185], v145 offset:54272
	ds_read_b128 v[186:189], v145 offset:55296
	ds_read_b128 v[190:193], v145 offset:56320
	global_load_lds_dwordx4 v[140:141], off
	v_lshl_add_u64 v[140:141], v[238:239], 0, s[36:37]
	s_mov_b32 m0, s29
	s_nop 0
	global_load_lds_dwordx4 v[140:141], off
	s_barrier
	s_waitcnt lgkmcnt(0)
	s_waitcnt lgkmcnt(0)
	v_mfma_f32_16x16x32_bf16 v[62:65], v[146:149], v[162:165], v[62:65]
	v_mfma_f32_16x16x32_bf16 v[58:61], v[154:157], v[162:165], v[58:61]
	v_mfma_f32_16x16x32_bf16 v[50:53], v[146:149], v[170:173], v[50:53]
	v_mfma_f32_16x16x32_bf16 v[42:45], v[154:157], v[170:173], v[42:45]
	v_mfma_f32_16x16x32_bf16 v[34:37], v[146:149], v[178:181], v[34:37]
	v_mfma_f32_16x16x32_bf16 v[26:29], v[154:157], v[178:181], v[26:29]
	v_mfma_f32_16x16x32_bf16 v[18:21], v[146:149], v[186:189], v[18:21]
	v_mfma_f32_16x16x32_bf16 v[10:13], v[154:157], v[186:189], v[10:13]
	v_mfma_f32_16x16x32_bf16 v[62:65], v[150:153], v[166:169], v[62:65]
	v_mfma_f32_16x16x32_bf16 v[58:61], v[158:161], v[166:169], v[58:61]
	v_mfma_f32_16x16x32_bf16 v[50:53], v[150:153], v[174:177], v[50:53]
	v_mfma_f32_16x16x32_bf16 v[42:45], v[158:161], v[174:177], v[42:45]
	v_mfma_f32_16x16x32_bf16 v[34:37], v[150:153], v[182:185], v[34:37]
	v_mfma_f32_16x16x32_bf16 v[26:29], v[158:161], v[182:185], v[26:29]
	v_mfma_f32_16x16x32_bf16 v[18:21], v[150:153], v[190:193], v[18:21]
	v_mfma_f32_16x16x32_bf16 v[10:13], v[158:161], v[190:193], v[10:13]
	s_barrier
	s_add_u32 s50, s50, 0x80080
	s_addc_u32 s51, s51, 0
	s_add_i32 s56, s57, s76
	v_lshl_add_u64 v[140:141], s[50:51], 0, v[210:211]
	s_mov_b32 m0, s56
	s_nop 0
	global_load_lds_dwordx4 v[140:141], off
	v_lshl_add_u64 v[140:141], s[50:51], 0, v[130:131]
	s_add_i32 m0, s56, 0x2000
	s_nop 0
	global_load_lds_dwordx4 v[140:141], off
	s_waitcnt vmcnt(6)
	s_barrier
	v_mfma_f32_16x16x32_bf16 v[54:57], v[194:197], v[162:165], v[54:57]
	v_mfma_f32_16x16x32_bf16 v[46:49], v[202:205], v[162:165], v[46:49]
	v_mfma_f32_16x16x32_bf16 v[38:41], v[194:197], v[170:173], v[38:41]
	v_mfma_f32_16x16x32_bf16 v[30:33], v[202:205], v[170:173], v[30:33]
	v_mfma_f32_16x16x32_bf16 v[22:25], v[194:197], v[178:181], v[22:25]
	v_mfma_f32_16x16x32_bf16 v[14:17], v[202:205], v[178:181], v[14:17]
	v_mfma_f32_16x16x32_bf16 v[6:9], v[194:197], v[186:189], v[6:9]
	v_mfma_f32_16x16x32_bf16 v[2:5], v[202:205], v[186:189], v[2:5]
	v_mfma_f32_16x16x32_bf16 v[54:57], v[198:201], v[166:169], v[54:57]
	v_mfma_f32_16x16x32_bf16 v[46:49], v[234:237], v[166:169], v[46:49]
	v_mfma_f32_16x16x32_bf16 v[38:41], v[198:201], v[174:177], v[38:41]
	v_mfma_f32_16x16x32_bf16 v[30:33], v[234:237], v[174:177], v[30:33]
	v_mfma_f32_16x16x32_bf16 v[22:25], v[198:201], v[182:185], v[22:25]
	v_mfma_f32_16x16x32_bf16 v[14:17], v[234:237], v[182:185], v[14:17]
	v_mfma_f32_16x16x32_bf16 v[6:9], v[198:201], v[190:193], v[6:9]
	v_mfma_f32_16x16x32_bf16 v[2:5], v[234:237], v[190:193], v[2:5]
	s_add_i32 s61, s61, 2
	s_add_u32 s0, s0, 0x100
	s_addc_u32 s1, s1, 0
	s_add_u32 s52, s52, 0x100
	s_addc_u32 s53, s53, 0
	s_cmp_gt_u32 s61, 29
	s_barrier
	s_cbranch_scc0 .LBB0_612
	v_lshl_add_u32 v146, s60, 8, v142
	v_lshl_or_b32 v140, s42, 8, v144
	v_ashrrev_i32_e32 v141, 31, v140
	v_ashrrev_i32_e32 v147, 31, v146
	v_lshl_add_u64 v[148:149], v[140:141], 1, s[8:9]
	v_lshlrev_b64 v[140:141], 11, v[146:147]
	v_lshl_add_u64 v[140:141], v[148:149], 0, v[140:141]
	v_pk_add_f32 v[128:129], v[128:129], 0 op_sel_hi:[1,0]
	v_pk_add_f32 v[126:127], v[126:127], 0 op_sel_hi:[1,0]
	v_pk_add_f32 v[150:151], v[124:125], 0 op_sel_hi:[1,0]
	v_pk_add_f32 v[124:125], v[122:123], 0 op_sel_hi:[1,0]
	v_cvt_pk_bf16_f32 v122, v126, v127
	v_cvt_pk_bf16_f32 v123, v128, v129
	v_pk_add_f32 v[118:119], v[118:119], 0 op_sel_hi:[1,0]
	v_cvt_pk_bf16_f32 v124, v124, v125
	v_cvt_pk_bf16_f32 v125, v150, v151
	global_store_dwordx4 v[140:141], v[122:125], off
	v_pk_add_f32 v[120:121], v[120:121], 0 op_sel_hi:[1,0]
	v_pk_add_f32 v[114:115], v[114:115], 0 op_sel_hi:[1,0]
	v_pk_add_f32 v[122:123], v[112:113], 0 op_sel_hi:[1,0]
	v_pk_add_f32 v[112:113], v[110:111], 0 op_sel_hi:[1,0]
	v_cvt_pk_bf16_f32 v110, v118, v119
	v_cvt_pk_bf16_f32 v111, v120, v121
	v_pk_add_f32 v[102:103], v[102:103], 0 op_sel_hi:[1,0]
	v_cvt_pk_bf16_f32 v112, v112, v113
	v_cvt_pk_bf16_f32 v113, v122, v123
	global_store_dwordx4 v[140:141], v[110:113], off offset:256
	v_pk_add_f32 v[104:105], v[104:105], 0 op_sel_hi:[1,0]
	v_pk_add_f32 v[98:99], v[98:99], 0 op_sel_hi:[1,0]
	v_or_b32_e32 v110, 16, v146
	v_ashrrev_i32_e32 v111, 31, v110
	v_lshlrev_b64 v[110:111], 11, v[110:111]
	v_lshl_add_u64 v[110:111], v[148:149], 0, v[110:111]
	v_pk_add_f32 v[112:113], v[116:117], 0 op_sel_hi:[1,0]
	v_pk_add_f32 v[116:117], v[108:109], 0 op_sel_hi:[1,0]
	v_pk_add_f32 v[108:109], v[106:107], 0 op_sel_hi:[1,0]
	v_cvt_pk_bf16_f32 v106, v114, v115
	v_cvt_pk_bf16_f32 v107, v112, v113
	v_pk_add_f32 v[86:87], v[86:87], 0 op_sel_hi:[1,0]
	v_cvt_pk_bf16_f32 v108, v108, v109
	v_cvt_pk_bf16_f32 v109, v116, v117
	global_store_dwordx4 v[110:111], v[106:109], off
	v_pk_add_f32 v[88:89], v[88:89], 0 op_sel_hi:[1,0]
	v_pk_add_f32 v[82:83], v[82:83], 0 op_sel_hi:[1,0]
	v_pk_add_f32 v[106:107], v[96:97], 0 op_sel_hi:[1,0]
	v_pk_add_f32 v[96:97], v[94:95], 0 op_sel_hi:[1,0]
	v_cvt_pk_bf16_f32 v94, v102, v103
	v_cvt_pk_bf16_f32 v95, v104, v105
	v_pk_add_f32 v[72:73], v[72:73], 0 op_sel_hi:[1,0]
	v_cvt_pk_bf16_f32 v96, v96, v97
	v_cvt_pk_bf16_f32 v97, v106, v107
	global_store_dwordx4 v[110:111], v[94:97], off offset:256
	v_pk_add_f32 v[70:71], v[70:71], 0 op_sel_hi:[1,0]
	s_mov_b64 s[0:1], 0x40000
	v_or_b32_e32 v94, 32, v146
	v_ashrrev_i32_e32 v95, 31, v94
	v_lshlrev_b64 v[94:95], 11, v[94:95]
	v_lshl_add_u64 v[94:95], v[148:149], 0, v[94:95]
	v_pk_add_f32 v[96:97], v[100:101], 0 op_sel_hi:[1,0]
	v_pk_add_f32 v[100:101], v[92:93], 0 op_sel_hi:[1,0]
	v_pk_add_f32 v[92:93], v[90:91], 0 op_sel_hi:[1,0]
	v_cvt_pk_bf16_f32 v90, v98, v99
	v_cvt_pk_bf16_f32 v91, v96, v97
	v_pk_add_f32 v[62:63], v[62:63], 0 op_sel_hi:[1,0]
	v_cvt_pk_bf16_f32 v92, v92, v93
	v_cvt_pk_bf16_f32 v93, v100, v101
	global_store_dwordx4 v[94:95], v[90:93], off
	v_pk_add_f32 v[64:65], v[64:65], 0 op_sel_hi:[1,0]
	v_pk_add_f32 v[56:57], v[56:57], 0 op_sel_hi:[1,0]
	v_pk_add_f32 v[90:91], v[80:81], 0 op_sel_hi:[1,0]
	v_pk_add_f32 v[80:81], v[78:79], 0 op_sel_hi:[1,0]
	v_cvt_pk_bf16_f32 v78, v86, v87
	v_cvt_pk_bf16_f32 v79, v88, v89
	v_pk_add_f32 v[54:55], v[54:55], 0 op_sel_hi:[1,0]
	v_cvt_pk_bf16_f32 v80, v80, v81
	v_cvt_pk_bf16_f32 v81, v90, v91
	global_store_dwordx4 v[94:95], v[78:81], off offset:256
	v_pk_add_f32 v[50:51], v[50:51], 0 op_sel_hi:[1,0]
	v_pk_add_f32 v[40:41], v[40:41], 0 op_sel_hi:[1,0]
	v_or_b32_e32 v78, 48, v146
	v_ashrrev_i32_e32 v79, 31, v78
	v_lshlrev_b64 v[78:79], 11, v[78:79]
	v_lshl_add_u64 v[78:79], v[148:149], 0, v[78:79]
	v_pk_add_f32 v[80:81], v[84:85], 0 op_sel_hi:[1,0]
	v_pk_add_f32 v[84:85], v[76:77], 0 op_sel_hi:[1,0]
	v_pk_add_f32 v[76:77], v[74:75], 0 op_sel_hi:[1,0]
	v_cvt_pk_bf16_f32 v74, v82, v83
	v_cvt_pk_bf16_f32 v75, v80, v81
	v_pk_add_f32 v[38:39], v[38:39], 0 op_sel_hi:[1,0]
	v_cvt_pk_bf16_f32 v76, v76, v77
	v_cvt_pk_bf16_f32 v77, v84, v85
	global_store_dwordx4 v[78:79], v[74:77], off
	v_pk_add_f32 v[34:35], v[34:35], 0 op_sel_hi:[1,0]
	v_pk_add_f32 v[24:25], v[24:25], 0 op_sel_hi:[1,0]
	v_pk_add_f32 v[74:75], v[68:69], 0 op_sel_hi:[1,0]
	v_pk_add_f32 v[68:69], v[66:67], 0 op_sel_hi:[1,0]
	v_cvt_pk_bf16_f32 v66, v70, v71
	v_cvt_pk_bf16_f32 v67, v72, v73
	v_pk_add_f32 v[22:23], v[22:23], 0 op_sel_hi:[1,0]
	v_cvt_pk_bf16_f32 v68, v68, v69
	v_cvt_pk_bf16_f32 v69, v74, v75
	global_store_dwordx4 v[78:79], v[66:69], off offset:256
	v_pk_add_f32 v[18:19], v[18:19], 0 op_sel_hi:[1,0]
	s_mov_b32 s42, s10
	v_lshl_add_u64 v[66:67], v[140:141], 0, s[0:1]
	s_mov_b32 s0, 0x40000
	v_pk_add_f32 v[68:69], v[60:61], 0 op_sel_hi:[1,0]
	v_pk_add_f32 v[60:61], v[58:59], 0 op_sel_hi:[1,0]
	v_cvt_pk_bf16_f32 v58, v62, v63
	v_add_co_u32_e32 v62, vcc, s0, v140
	v_cvt_pk_bf16_f32 v59, v64, v65
	v_cvt_pk_bf16_f32 v60, v60, v61
	v_cvt_pk_bf16_f32 v61, v68, v69
	s_mov_b64 s[0:1], 0x48000
	s_nop 0
	v_addc_co_u32_e32 v63, vcc, 0, v141, vcc
	global_store_dwordx4 v[62:63], v[58:61], off
	s_mov_b32 s60, s24
	s_mov_b64 s[50:51], s[34:35]
	v_pk_add_f32 v[58:59], v[48:49], 0 op_sel_hi:[1,0]
	v_pk_add_f32 v[48:49], v[46:47], 0 op_sel_hi:[1,0]
	v_cvt_pk_bf16_f32 v46, v54, v55
	v_cvt_pk_bf16_f32 v47, v56, v57
	s_mov_b64 s[62:63], s[40:41]
	v_cvt_pk_bf16_f32 v48, v48, v49
	v_cvt_pk_bf16_f32 v49, v58, v59
	global_store_dwordx4 v[66:67], v[46:49], off offset:256
	v_pk_add_f32 v[8:9], v[8:9], 0 op_sel_hi:[1,0]
	v_pk_add_f32 v[6:7], v[6:7], 0 op_sel_hi:[1,0]
	v_lshl_add_u64 v[46:47], v[140:141], 0, s[0:1]
	v_pk_add_f32 v[48:49], v[52:53], 0 op_sel_hi:[1,0]
	s_mov_b32 s0, 0x48000
	v_pk_add_f32 v[52:53], v[44:45], 0 op_sel_hi:[1,0]
	v_pk_add_f32 v[44:45], v[42:43], 0 op_sel_hi:[1,0]
	v_cvt_pk_bf16_f32 v42, v50, v51
	v_cvt_pk_bf16_f32 v43, v48, v49
	v_add_co_u32_e32 v48, vcc, s0, v140
	v_cvt_pk_bf16_f32 v44, v44, v45
	v_cvt_pk_bf16_f32 v45, v52, v53
	s_mov_b64 s[0:1], 0x50000
	s_nop 0
	v_addc_co_u32_e32 v49, vcc, 0, v141, vcc
	global_store_dwordx4 v[48:49], v[42:45], off
	s_nop 1
	v_pk_add_f32 v[42:43], v[32:33], 0 op_sel_hi:[1,0]
	v_pk_add_f32 v[32:33], v[30:31], 0 op_sel_hi:[1,0]
	v_cvt_pk_bf16_f32 v30, v38, v39
	v_cvt_pk_bf16_f32 v31, v40, v41
	s_nop 0
	v_cvt_pk_bf16_f32 v32, v32, v33
	v_cvt_pk_bf16_f32 v33, v42, v43
	global_store_dwordx4 v[46:47], v[30:33], off offset:256
	s_nop 1
	v_lshl_add_u64 v[30:31], v[140:141], 0, s[0:1]
	v_pk_add_f32 v[32:33], v[36:37], 0 op_sel_hi:[1,0]
	s_mov_b32 s0, 0x50000
	v_pk_add_f32 v[36:37], v[28:29], 0 op_sel_hi:[1,0]
	v_pk_add_f32 v[28:29], v[26:27], 0 op_sel_hi:[1,0]
	v_cvt_pk_bf16_f32 v26, v34, v35
	v_cvt_pk_bf16_f32 v27, v32, v33
	v_add_co_u32_e32 v32, vcc, s0, v140
	v_cvt_pk_bf16_f32 v28, v28, v29
	v_cvt_pk_bf16_f32 v29, v36, v37
	s_mov_b64 s[0:1], 0x58000
	s_nop 0
	v_addc_co_u32_e32 v33, vcc, 0, v141, vcc
	global_store_dwordx4 v[32:33], v[26:29], off
	s_nop 1
	v_pk_add_f32 v[26:27], v[16:17], 0 op_sel_hi:[1,0]
	v_pk_add_f32 v[16:17], v[14:15], 0 op_sel_hi:[1,0]
	v_cvt_pk_bf16_f32 v14, v22, v23
	v_cvt_pk_bf16_f32 v15, v24, v25
	s_nop 0
	v_cvt_pk_bf16_f32 v16, v16, v17
	v_cvt_pk_bf16_f32 v17, v26, v27
	global_store_dwordx4 v[30:31], v[14:17], off offset:256
	s_nop 1
	v_lshl_add_u64 v[14:15], v[140:141], 0, s[0:1]
	v_pk_add_f32 v[16:17], v[20:21], 0 op_sel_hi:[1,0]
	s_mov_b32 s0, 0x58000
	v_pk_add_f32 v[20:21], v[12:13], 0 op_sel_hi:[1,0]
	v_pk_add_f32 v[12:13], v[10:11], 0 op_sel_hi:[1,0]
	v_cvt_pk_bf16_f32 v10, v18, v19
	v_cvt_pk_bf16_f32 v11, v16, v17
	v_add_co_u32_e32 v16, vcc, s0, v140
	v_cvt_pk_bf16_f32 v12, v12, v13
	v_cvt_pk_bf16_f32 v13, v20, v21
	s_nop 1
	v_addc_co_u32_e32 v17, vcc, 0, v141, vcc
	global_store_dwordx4 v[16:17], v[10:13], off
	s_and_b64 vcc, exec, s[38:39]
	s_nop 0
	v_pk_add_f32 v[10:11], v[4:5], 0 op_sel_hi:[1,0]
	v_pk_add_f32 v[4:5], v[2:3], 0 op_sel_hi:[1,0]
	v_cvt_pk_bf16_f32 v2, v6, v7
	v_cvt_pk_bf16_f32 v3, v8, v9
	s_nop 0
	v_cvt_pk_bf16_f32 v4, v4, v5
	v_cvt_pk_bf16_f32 v5, v10, v11
	global_store_dwordx4 v[14:15], v[2:5], off offset:256
	s_cbranch_vccz .LBB0_609
	s_waitcnt vmcnt(0)
	v_readlane_b32 s28, v255, 39
	s_cmpk_gt_u32 s33, 0xff
	v_readlane_b32 s29, v255, 40
	s_cbranch_scc1 .LBB0_616
	s_barrier

.LBB0_617:
	s_setprio 0
	s_mov_b32 s5, 0x8000
	v_readlane_b32 s6, v255, 49
	v_readlane_b32 s76, v255, 56
	v_mov_b32_e32 v2, v0
	v_readlane_b32 s0, v253, 52
	s_nop 0
	s_sub_i32 s0, s0, 64
	s_add_i32 s6, s6, 0xffffffc0
	s_cmp_lt_i32 s0, 0
	s_cbranch_scc1 .Lcvtx_skip
	v_ashrrev_i32_e32 v3, 6, v2
	s_nop 0
	v_add_u32_e32 v40, s0, v3
	v_cmp_gt_i32_e32 vcc, s5, v40
	s_and_saveexec_b64 s[10:11], vcc
	s_cbranch_execz .Lcvtx_done
	v_and_b32_e32 v3, 63, v2
	v_lshlrev_b32_e32 v4, 5, v3
	v_cmp_eq_u32_e64 s[0:1], 0, v3
	v_lshlrev_b32_e32 v3, 11, v2
	v_lshlrev_b32_e32 v2, 4, v2
	s_lshl_b32 s80, s76, 14
	v_and_b32_e32 v34, 0x1c000, v3
	v_mov_b32_e32 v35, v211
	v_and_b32_e32 v36, 0x70, v2
	v_mov_b32_e32 v37, v211
	s_mov_b64 s[54:55], 0
	v_lshlrev_b32_e32 v210, 2, v4
	s_branch .Lcvtx_loop
